# baseline (speedup 1.0000x reference)
.LBB0_30:
	v_mov_b32_e32 v209, v245
	v_mul_u32_u24_e32 v101, 0x4540, v213
	v_add_u32_e32 v101, v101, v210
	v_mov_b32_e32 v253, v210
	v_add_u32_e32 v254, 0xcfc0, v210
	v_add_u32_e32 v255, 0x19f80, v210
	s_waitcnt vmcnt(0)
	ds_write_b128 v101, v[104:107] offset:9216
	ds_write_b128 v101, v[108:111] offset:10240
	ds_write_b128 v101, v[112:115] offset:11264
	ds_write_b128 v101, v[116:119] offset:12288
	ds_write_b128 v101, v[120:123] offset:13312
	v_readfirstlane_b32 s0, v213
	s_cmp_lt_i32 s0, 3
	s_waitcnt lgkmcnt(0)
	s_barrier
	s_cbranch_scc0 .LBB0_33
	v_mov_b32_e32 v83, 0
	v_mov_b32_e32 v211, v83
	v_lshl_add_u64 v[156:157], s[36:37], 0, v[210:211]
	s_movk_i32 s0, 0x3000
	v_add_co_u32_e32 v68, vcc, s0, v156
	s_movk_i32 s0, 0x2000
	s_nop 0
	v_addc_co_u32_e32 v69, vcc, 0, v157, vcc
	ds_read_b128 v[0:3], v253 offset:8192
	v_add_co_u32_e32 v70, vcc, s0, v156
	s_movk_i32 s0, 0x1000
	s_nop 0
	v_addc_co_u32_e32 v71, vcc, 0, v157, vcc
	ds_read_b128 v[16:19], v253 offset:9216
	ds_read_b128 v[56:59], v253
	ds_read_b128 v[52:55], v253 offset:1024
	ds_read_b128 v[48:51], v253 offset:2048
	ds_read_b128 v[44:47], v253 offset:3072
	v_add_co_u32_e32 v20, vcc, s0, v156
	s_movk_i32 s0, 0x50
	s_nop 0
	v_addc_co_u32_e32 v21, vcc, 0, v157, vcc
	ds_read_b128 v[40:43], v253 offset:4096
	ds_read_b128 v[36:39], v253 offset:5120
	ds_read_b128 v[32:35], v253 offset:6144
	ds_read_b128 v[60:63], v253 offset:12288
	ds_read_b128 v[72:75], v253 offset:7168
	ds_read_b128 v[76:79], v253 offset:10240
	v_lshl_or_b32 v20, v213, 5, v212
	v_mov_b32_e32 v21, 0x4f
	v_cmp_gt_u32_e64 s[0:1], s0, v20
	s_lshl_b32 s2, s2, 2
	s_movk_i32 s3, 0x4000
	v_cndmask_b32_e64 v100, v21, v20, s[0:1]
	v_lshl_or_b32 v64, v100, 7, v208
	v_add_u32_e32 v127, 0x22a00, v64
	ds_read_b128 v[64:67], v127
	ds_read_b128 v[84:87], v127 offset:32
	s_mov_b32 s9, 0x66666667
	v_add_co_u32_e32 v108, vcc, s3, v156
	s_movk_i32 s10, 0x5000
	s_nop 0
	v_addc_co_u32_e32 v109, vcc, 0, v157, vcc
	v_add_co_u32_e32 v152, vcc, s10, v156
	v_lshlrev_b32_e32 v82, 1, v214
	s_nop 0
	v_addc_co_u32_e32 v153, vcc, 0, v157, vcc
	v_mov_b32_e32 v126, 0x3727c5ac
	s_mov_b32 s8, 0xf800000
	v_mov_b32_e32 v208, 0x260
	v_mov_b32_e32 v80, s26
	v_mov_b32_e32 v81, s27
	s_and_b64 s[0:1], s[4:5], s[0:1]
	s_waitcnt lgkmcnt(12)
	v_mfma_f32_32x32x16_f16 v[16:31], v[16:19], v[96:99], 0
	v_mfma_f32_32x32x16_f16 v[0:15], v[0:3], v[96:99], 0
	s_waitcnt lgkmcnt(1)
	v_mfma_f32_32x32x16_f16 v[0:15], v[56:59], v[64:67], v[0:15]
	s_waitcnt lgkmcnt(1)
	v_mfma_f32_32x32x16_f16 v[16:31], v[52:55], v[64:67], v[16:31]
	v_mul_lo_u16_e32 v52, 0xcd, v100
	v_lshrrev_b16_e32 v52, 10, v52
	v_lshlrev_b32_e32 v102, 10, v52
	v_lshrrev_b32_e32 v101, 2, v52
	v_sub_u32_e32 v103, s2, v52
	s_waitcnt lgkmcnt(0)
	v_mfma_f32_32x32x16_f16 v[0:15], v[48:51], v[84:87], v[0:15]
	ds_read_b128 v[48:51], v127 offset:64
	ds_read_b128 v[88:91], v127 offset:96
	s_waitcnt lgkmcnt(2)
	v_mfma_f32_32x32x16_f16 v[16:31], v[44:47], v[84:87], v[16:31]
	ds_read_b128 v[84:87], v253 offset:18752
	ds_read_b128 v[92:95], v253 offset:19776
	ds_read_b128 v[120:123], v253 offset:11264
	ds_read_b128 v[52:55], v253 offset:13312
	ds_read_b128 v[56:59], v253 offset:14336
	ds_read_b128 v[44:47], v253 offset:15360
	ds_read_b128 v[64:67], v253 offset:16384
	s_waitcnt lgkmcnt(8)
	v_mfma_f32_32x32x16_f16 v[0:15], v[40:43], v[48:51], v[0:15]
	v_and_b32_e32 v40, 0xc00, v102
	v_add3_u32 v40, v103, v101, v40
	v_mad_u64_u32 v[158:159], s[2:3], v40, 5, v[100:101]
	v_mul_hi_i32 v42, v158, s9
	v_lshlrev_b32_e32 v40, 6, v158
	v_ashrrev_i32_e32 v41, 31, v40
	s_waitcnt lgkmcnt(8)
	v_mfma_f32_32x32x16_f16 v[16:31], v[36:39], v[48:51], v[16:31]
	v_lshrrev_b32_e32 v38, 31, v42
	v_ashrrev_i32_e32 v39, 1, v42
	v_add_u32_e32 v159, v39, v38
	v_lshlrev_b32_e32 v68, 6, v159
	v_ashrrev_i32_e32 v69, 31, v68
	v_lshl_add_u64 v[48:49], v[68:69], 2, s[24:25]
	v_lshl_add_u64 v[36:37], v[40:41], 1, s[6:7]
	s_waitcnt lgkmcnt(7)
	v_mfma_f32_32x32x16_f16 v[0:15], v[32:35], v[88:91], v[0:15]
	v_lshl_add_u64 v[70:71], v[36:37], 0, v[82:83]
	v_lshlrev_b32_e32 v82, 2, v216
	v_lshl_add_u64 v[116:117], v[48:49], 0, v[82:83]
	global_load_dwordx4 v[32:35], v82, s[28:29]
	global_load_dwordx4 v[36:39], v82, s[28:29] offset:32
	global_load_dwordx4 v[40:43], v82, s[28:29] offset:64
	global_load_dwordx4 v[128:131], v82, s[28:29] offset:96
	v_add_u32_e32 v68, 0x40000, v68
	s_mov_b32 s6, 0xd000
	s_mov_b32 s7, 0xc000
	s_waitcnt lgkmcnt(7)
	v_mfma_f32_32x32x16_f16 v[16:31], v[72:75], v[88:91], v[16:31]
	s_nop 11
	v_add_f32_e32 v69, v0, v16
	v_add_f32_e32 v90, v1, v17
	v_add_f32_e32 v69, 0, v69
	v_add_f32_e32 v91, v2, v18
	v_add_f32_e32 v69, v90, v69
	v_add_f32_e32 v100, v3, v19
	v_add_f32_e32 v69, v91, v69
	v_add_f32_e32 v101, v4, v20
	v_add_f32_e32 v69, v100, v69
	v_add_f32_e32 v102, v5, v21
	v_add_f32_e32 v69, v101, v69
	v_pk_add_f32 v[48:49], v[6:7], v[22:23]
	v_add_f32_e32 v69, v102, v69
	v_add_f32_e32 v48, v48, v69
	v_pk_add_f32 v[50:51], v[8:9], v[24:25]
	v_add_f32_e32 v48, v49, v48
	v_add_f32_e32 v48, v50, v48
	v_pk_add_f32 v[72:73], v[10:11], v[26:27]
	v_add_f32_e32 v48, v51, v48
	v_add_f32_e32 v48, v72, v48
	v_pk_add_f32 v[74:75], v[12:13], v[28:29]
	v_add_f32_e32 v48, v73, v48
	v_add_f32_e32 v48, v74, v48
	v_pk_add_f32 v[88:89], v[14:15], v[30:31]
	v_add_f32_e32 v48, v75, v48
	v_add_f32_e32 v48, v88, v48
	v_add_f32_e32 v69, v89, v48
	global_load_dwordx4 v[48:51], v[116:117], off
	global_load_dwordx4 v[88:91], v[116:117], off offset:32
	global_load_dwordx4 v[132:135], v[116:117], off offset:64
	global_load_dwordx4 v[136:139], v[116:117], off offset:96
	global_load_dwordx4 v[104:107], v[70:71], off
	global_load_dwordx4 v[100:103], v[70:71], off offset:32
	global_load_dwordx4 v[140:143], v82, s[28:29] offset:128
	global_load_dwordx4 v[144:147], v82, s[28:29] offset:160
	global_load_dwordx4 v[148:151], v[116:117], off offset:128
	global_load_dwordx4 v[160:163], v82, s[28:29] offset:192
	global_load_dwordx4 v[164:167], v[116:117], off offset:160
	global_load_dwordx4 v[168:171], v[116:117], off offset:192
	ds_read_b128 v[172:175], v253 offset:17728
	s_waitcnt lgkmcnt(8)
	v_mov_b32_e32 v72, v69
	s_nop 1
	v_permlane32_swap_b32_e32 v69, v72
	s_nop 0
	v_add_f32_e32 v69, v69, v72
	v_mul_f32_e32 v72, 0x3c800000, v69
	v_pk_add_f32 v[124:125], v[30:31], v[72:73] op_sel_hi:[1,0] neg_lo:[0,1] neg_hi:[0,1]
	v_pk_add_f32 v[154:155], v[14:15], v[72:73] op_sel_hi:[1,0] neg_lo:[0,1] neg_hi:[0,1]
	v_pk_add_f32 v[184:185], v[28:29], v[72:73] op_sel_hi:[1,0] neg_lo:[0,1] neg_hi:[0,1]
	v_pk_add_f32 v[186:187], v[12:13], v[72:73] op_sel_hi:[1,0] neg_lo:[0,1] neg_hi:[0,1]
	v_pk_add_f32 v[188:189], v[26:27], v[72:73] op_sel_hi:[1,0] neg_lo:[0,1] neg_hi:[0,1]
	v_pk_add_f32 v[190:191], v[10:11], v[72:73] op_sel_hi:[1,0] neg_lo:[0,1] neg_hi:[0,1]
	v_pk_add_f32 v[192:193], v[24:25], v[72:73] op_sel_hi:[1,0] neg_lo:[0,1] neg_hi:[0,1]
	v_pk_add_f32 v[194:195], v[8:9], v[72:73] op_sel_hi:[1,0] neg_lo:[0,1] neg_hi:[0,1]
	v_pk_add_f32 v[196:197], v[22:23], v[72:73] op_sel_hi:[1,0] neg_lo:[0,1] neg_hi:[0,1]
	v_pk_add_f32 v[74:75], v[6:7], v[72:73] op_sel_hi:[1,0] neg_lo:[0,1] neg_hi:[0,1]
	v_pk_add_f32 v[198:199], v[20:21], v[72:73] op_sel_hi:[1,0] neg_lo:[0,1] neg_hi:[0,1]
	v_pk_add_f32 v[118:119], v[4:5], v[72:73] op_sel_hi:[1,0] neg_lo:[0,1] neg_hi:[0,1]
	v_pk_add_f32 v[200:201], v[18:19], v[72:73] op_sel_hi:[1,0] neg_lo:[0,1] neg_hi:[0,1]
	v_pk_add_f32 v[202:203], v[2:3], v[72:73] op_sel_hi:[1,0] neg_lo:[0,1] neg_hi:[0,1]
	v_pk_add_f32 v[204:205], v[16:17], v[72:73] op_sel_hi:[1,0] neg_lo:[0,1] neg_hi:[0,1]
	v_pk_add_f32 v[72:73], v[0:1], v[72:73] op_sel_hi:[1,0] neg_lo:[0,1] neg_hi:[0,1]
	global_load_dwordx4 v[112:115], v[70:71], off offset:64
	global_load_dwordx4 v[108:111], v[70:71], off offset:96
	global_load_dwordx4 v[176:179], v82, s[28:29] offset:224
	global_load_dwordx4 v[180:183], v[116:117], off offset:224
	v_fma_f32 v0, v72, v72, 0
	v_fmac_f32_e32 v0, v204, v204
	v_fmac_f32_e32 v0, v73, v73
	v_fmac_f32_e32 v0, v205, v205
	v_fmac_f32_e32 v0, v202, v202
	v_fmac_f32_e32 v0, v200, v200
	v_fmac_f32_e32 v0, v203, v203
	v_fmac_f32_e32 v0, v201, v201
	v_fmac_f32_e32 v0, v118, v118
	v_fmac_f32_e32 v0, v198, v198
	v_fmac_f32_e32 v0, v119, v119
	v_fmac_f32_e32 v0, v199, v199
	v_fmac_f32_e32 v0, v74, v74
	v_fmac_f32_e32 v0, v196, v196
	v_fmac_f32_e32 v0, v75, v75
	v_fmac_f32_e32 v0, v197, v197
	v_fmac_f32_e32 v0, v194, v194
	v_fmac_f32_e32 v0, v192, v192
	v_fmac_f32_e32 v0, v195, v195
	v_fmac_f32_e32 v0, v193, v193
	v_fmac_f32_e32 v0, v190, v190
	v_fmac_f32_e32 v0, v188, v188
	v_fmac_f32_e32 v0, v191, v191
	v_fmac_f32_e32 v0, v189, v189
	v_fmac_f32_e32 v0, v186, v186
	v_fmac_f32_e32 v0, v184, v184
	v_fmac_f32_e32 v0, v187, v187
	v_fmac_f32_e32 v0, v185, v185
	v_fmac_f32_e32 v0, v154, v154
	v_fmac_f32_e32 v0, v124, v124
	v_fmac_f32_e32 v0, v155, v155
	v_fmac_f32_e32 v0, v125, v125
	s_waitcnt lgkmcnt(8)
	v_mov_b32_e32 v1, v0
	s_nop 1
	v_permlane32_swap_b32_e32 v0, v1
	s_nop 0
	v_add_f32_e32 v0, v0, v1
	v_fmamk_f32 v0, v0, 0x3c800000, v126
	v_mul_f32_e32 v1, 0x4f800000, v0
	v_cmp_gt_f32_e32 vcc, s8, v0
	s_nop 1
	v_cndmask_b32_e32 v0, v0, v1, vcc
	v_sqrt_f32_e32 v1, v0
	s_nop 0
	v_add_u32_e32 v2, -1, v1
	v_fma_f32 v3, -v2, v1, v0
	v_cmp_ge_f32_e64 s[2:3], 0, v3
	v_add_u32_e32 v3, 1, v1
	s_nop 0
	v_cndmask_b32_e64 v2, v1, v2, s[2:3]
	v_fma_f32 v1, -v3, v1, v0
	v_cmp_lt_f32_e64 s[2:3], 0, v1
	s_nop 1
	v_cndmask_b32_e64 v1, v2, v3, s[2:3]
	v_mul_f32_e32 v2, 0x37800000, v1
	v_cndmask_b32_e32 v1, v1, v2, vcc
	v_cmp_class_f32_e32 vcc, v0, v208
	s_nop 1
	v_cndmask_b32_e32 v69, v1, v0, vcc
	v_div_scale_f32 v16, s[2:3], v69, v69, 1.0
	v_rcp_f32_e32 v206, v16
	s_waitcnt lgkmcnt(7)
	v_mfma_f32_32x32x16_f16 v[0:15], v[84:87], v[96:99], 0
	ds_read_b128 v[84:87], v127 offset:10240
	s_mov_b32 s2, 0xa000
	v_fma_f32 v17, -v16, v206, 1.0
	v_fmac_f32_e32 v206, v17, v206
	v_div_scale_f32 v17, vcc, 1.0, v69, 1.0
	v_mul_f32_e32 v70, v17, v206
	v_fma_f32 v18, -v16, v70, v17
	v_fmac_f32_e32 v70, v18, v206
	v_fma_f32 v71, -v16, v70, v17
	s_waitcnt lgkmcnt(7)
	v_mfma_f32_32x32x16_f16 v[16:31], v[92:95], v[96:99], 0
	ds_read_b128 v[92:95], v127 offset:10272
	v_div_fmas_f32 v70, v71, v206, v70
	v_div_fixup_f32 v70, v70, v69, 1.0
	v_mul_f32_e64 v210, v118, v70
	v_mul_f32_e64 v211, v119, v70
	v_pk_mul_f32 v[206:207], v[74:75], v[70:71] op_sel_hi:[1,0]
	v_pk_mul_f32 v[74:75], v[202:203], v[70:71] op_sel_hi:[1,0]
	s_waitcnt vmcnt(14) lgkmcnt(3)
	v_pk_fma_f32 v[36:37], v[210:211], v[36:37], v[88:89]
	s_waitcnt vmcnt(14) lgkmcnt(1)
	v_mfma_f32_32x32x16_f16 v[0:15], v[76:79], v[84:87], v[0:15]
	v_fma_f32 v34, v74, v34, v50
	v_fma_f32 v35, v75, v35, v51
	v_fma_f32 v38, v206, v38, v90
	v_fma_f32 v39, v207, v39, v91
	v_cvt_pk_f16_f32 v50, v36, v37
	v_pk_mul_f32 v[36:37], v[154:155], v[70:71] op_sel_hi:[1,0]
	v_cvt_pk_f16_f32 v51, v38, v39
	v_pk_mul_f32 v[38:39], v[186:187], v[70:71] op_sel_hi:[1,0]
	s_waitcnt vmcnt(12) lgkmcnt(1)
	v_pk_fma_f32 v[36:37], v[36:37], v[130:131], v[138:139]
	v_mfma_f32_32x32x16_f16 v[16:31], v[120:123], v[84:87], v[16:31]
	ds_read_b128 v[84:87], v127 offset:10336
	v_mul_f32_e64 v72, v72, v70
	v_mul_f32_e64 v73, v73, v70
	v_mul_f32_e64 v88, v184, v70
	v_mul_f32_e64 v89, v185, v70
	v_pk_fma_f32 v[32:33], v[72:73], v[32:33], v[48:49]
	v_cvt_pk_f16_f32 v49, v34, v35
	v_cvt_pk_f16_f32 v48, v32, v33
	v_pk_mul_f32 v[32:33], v[190:191], v[70:71] op_sel_hi:[1,0]
	s_waitcnt vmcnt(12) lgkmcnt(1)
	v_mfma_f32_32x32x16_f16 v[0:15], v[60:63], v[92:95], v[0:15]
	v_fma_f32 v60, v38, v128, v136
	v_fma_f32 v61, v39, v129, v137
	v_mul_f32_e64 v62, v204, v70
	v_mul_f32_e64 v63, v205, v70
	v_mul_f32_e64 v34, v194, v70
	v_mul_f32_e64 v35, v195, v70
	s_waitcnt vmcnt(7) lgkmcnt(1)
	v_pk_fma_f32 v[62:63], v[62:63], v[140:141], v[148:149]
	v_pk_fma_f32 v[40:41], v[34:35], v[40:41], v[132:133]
	v_pk_fma_f32 v[42:43], v[32:33], v[42:43], v[134:135]
	global_load_dwordx4 v[116:119], v82, s[30:31]
	global_load_dwordx4 v[72:75], v82, s[30:31] offset:32
	v_mfma_f32_32x32x16_f16 v[16:31], v[52:55], v[92:95], v[16:31]
	v_cvt_pk_f16_f32 v55, v36, v37
	ds_read_b128 v[36:39], v127 offset:10304
	v_cvt_pk_f16_f32 v54, v60, v61
	v_mul_f32_e64 v60, v200, v70
	v_mul_f32_e64 v61, v201, v70
	global_load_dwordx4 v[76:79], v82, s[30:31] offset:64
	global_load_dwordx4 v[32:35], v82, s[30:31] offset:96
	v_pk_fma_f32 v[60:61], v[60:61], v[142:143], v[150:151]
	s_waitcnt vmcnt(11) lgkmcnt(0)
	v_mfma_f32_32x32x16_f16 v[0:15], v[56:59], v[36:39], v[0:15]
	v_mul_f32_e64 v56, v196, v70
	v_mul_f32_e64 v57, v197, v70
	v_mul_f32_e64 v58, v198, v70
	v_mul_f32_e64 v59, v199, v70
	v_cvt_pk_f16_f32 v53, v42, v43
	v_cvt_pk_f16_f32 v52, v40, v41
	global_load_dwordx4 v[40:43], v82, s[30:31] offset:128
	v_mfma_f32_32x32x16_f16 v[16:31], v[44:47], v[36:39], v[16:31]
	s_waitcnt vmcnt(10) lgkmcnt(0)
	v_fma_f32 v38, v56, v146, v166
	v_fma_f32 v39, v57, v147, v167
	v_cvt_pk_f16_f32 v57, v60, v61
	v_mul_f32_e64 v60, v188, v70
	v_mul_f32_e64 v61, v189, v70
	v_cvt_pk_f16_f32 v56, v62, v63
	v_pk_mul_f32 v[62:63], v[124:125], v[70:71] op_sel_hi:[1,0]
	s_waitcnt vmcnt(9) lgkmcnt(0)
	v_pk_fma_f32 v[60:61], v[60:61], v[162:163], v[170:171]
	v_add_co_u32_e32 v170, vcc, s2, v156
	v_mfma_f32_32x32x16_f16 v[0:15], v[64:67], v[84:87], v[0:15]
	v_mul_f32_e64 v64, v192, v70
	v_mul_f32_e64 v65, v193, v70
	v_fma_f32 v36, v58, v144, v164
	v_fma_f32 v37, v59, v145, v165
	v_fma_f32 v136, v64, v160, v168
	v_fma_f32 v137, v65, v161, v169
	s_waitcnt vmcnt(5) lgkmcnt(0)
	v_pk_fma_f32 v[70:71], v[88:89], v[176:177], v[180:181]
	v_pk_fma_f32 v[62:63], v[62:63], v[178:179], v[182:183]
	v_addc_co_u32_e32 v171, vcc, 0, v157, vcc
	v_mfma_f32_32x32x16_f16 v[16:31], v[172:175], v[84:87], v[16:31]
	global_load_dwordx4 v[44:47], v82, s[30:31] offset:160
	v_cvt_pk_f16_f32 v59, v38, v39
	v_cvt_pk_f16_f32 v58, v36, v37
	global_load_dwordx4 v[36:39], v82, s[30:31] offset:192
	v_cvt_pk_f16_f32 v63, v62, v63
	v_cvt_pk_f16_f32 v62, v70, v71
	s_movk_i32 s2, 0x7000
	s_nop 4
	v_add_f32_e32 v64, v0, v16
	v_add_f32_e32 v64, 0, v64
	v_add_f32_e32 v65, v1, v17
	v_add_f32_e32 v64, v65, v64
	v_add_f32_e32 v65, v2, v18
	v_add_f32_e32 v64, v65, v64
	v_add_f32_e32 v65, v3, v19
	v_add_f32_e32 v64, v65, v64
	v_add_f32_e32 v65, v4, v20
	v_add_f32_e32 v64, v65, v64
	v_add_f32_e32 v65, v5, v21
	v_add_f32_e32 v66, v65, v64
	v_pk_add_f32 v[64:65], v[6:7], v[22:23]
	v_add_co_u32_e32 v184, vcc, s2, v156
	v_add_f32_e32 v64, v64, v66
	v_add_f32_e32 v66, v65, v64
	v_pk_add_f32 v[64:65], v[8:9], v[24:25]
	v_addc_co_u32_e32 v185, vcc, 0, v157, vcc
	v_add_f32_e32 v64, v64, v66
	v_add_f32_e32 v66, v65, v64
	v_pk_add_f32 v[64:65], v[10:11], v[26:27]
	s_movk_i32 s2, 0x6000
	v_add_f32_e32 v64, v64, v66
	v_add_f32_e32 v66, v65, v64
	v_pk_add_f32 v[64:65], v[12:13], v[28:29]
	v_add_co_u32_e32 v186, vcc, s2, v156
	v_add_f32_e32 v64, v64, v66
	v_add_f32_e32 v66, v65, v64
	v_pk_add_f32 v[64:65], v[14:15], v[30:31]
	v_addc_co_u32_e32 v187, vcc, 0, v157, vcc
	v_add_f32_e32 v64, v64, v66
	v_add_f32_e32 v69, v65, v64
	global_load_dwordx4 v[64:67], v82, s[30:31] offset:224
	v_cvt_pk_f16_f32 v61, v60, v61
	v_cvt_pk_f16_f32 v60, v136, v137
	s_waitcnt vmcnt(8) lgkmcnt(0)
	v_mov_b32_e32 v84, v69
	s_nop 1
	v_permlane32_swap_b32_e32 v69, v84
	s_nop 0
	v_add_f32_e32 v69, v69, v84
	v_mul_f32_e32 v92, 0x3c800000, v69
	v_ashrrev_i32_e32 v69, 31, v68
	v_lshl_add_u64 v[68:69], v[68:69], 2, s[24:25]
	v_lshl_add_u64 v[124:125], v[68:69], 0, v[82:83]
	global_load_dwordx4 v[140:143], v[124:125], off
	global_load_dwordx4 v[88:91], v[124:125], off offset:32
	global_load_dwordx4 v[84:87], v[124:125], off offset:64
	global_load_dwordx4 v[68:71], v[124:125], off offset:96
	v_pk_add_f32 v[180:181], v[10:11], v[92:93] op_sel_hi:[1,0] neg_lo:[0,1] neg_hi:[0,1]
	v_pk_add_f32 v[182:183], v[8:9], v[92:93] op_sel_hi:[1,0] neg_lo:[0,1] neg_hi:[0,1]
	v_pk_add_f32 v[8:9], v[2:3], v[92:93] op_sel_hi:[1,0] neg_lo:[0,1] neg_hi:[0,1]
	v_pk_add_f32 v[10:11], v[0:1], v[92:93] op_sel_hi:[1,0] neg_lo:[0,1] neg_hi:[0,1]
	ds_read_b128 v[0:3], v253 offset:37504
	v_pk_add_f32 v[178:179], v[12:13], v[92:93] op_sel_hi:[1,0] neg_lo:[0,1] neg_hi:[0,1]
	v_pk_add_f32 v[174:175], v[16:17], v[92:93] op_sel_hi:[1,0] neg_lo:[0,1] neg_hi:[0,1]
	v_fma_f32 v12, v10, v10, 0
	v_fmac_f32_e32 v12, v174, v174
	v_fmac_f32_e32 v12, v11, v11
	v_fmac_f32_e32 v12, v175, v175
	v_pk_add_f32 v[172:173], v[18:19], v[92:93] op_sel_hi:[1,0] neg_lo:[0,1] neg_hi:[0,1]
	v_fmac_f32_e32 v12, v8, v8
	ds_read_b128 v[144:147], v253 offset:20800
	ds_read_b128 v[148:151], v253 offset:22848
	v_fmac_f32_e32 v12, v172, v172
	v_fmac_f32_e32 v12, v9, v9
	v_pk_add_f32 v[4:5], v[4:5], v[92:93] op_sel_hi:[1,0] neg_lo:[0,1] neg_hi:[0,1]
	v_fmac_f32_e32 v12, v173, v173
	v_pk_add_f32 v[168:169], v[20:21], v[92:93] op_sel_hi:[1,0] neg_lo:[0,1] neg_hi:[0,1]
	v_fmac_f32_e32 v12, v4, v4
	v_fmac_f32_e32 v12, v168, v168
	v_fmac_f32_e32 v12, v5, v5
	v_pk_add_f32 v[6:7], v[6:7], v[92:93] op_sel_hi:[1,0] neg_lo:[0,1] neg_hi:[0,1]
	v_fmac_f32_e32 v12, v169, v169
	v_pk_add_f32 v[166:167], v[22:23], v[92:93] op_sel_hi:[1,0] neg_lo:[0,1] neg_hi:[0,1]
	v_fmac_f32_e32 v12, v6, v6
	v_fmac_f32_e32 v12, v166, v166
	v_fmac_f32_e32 v12, v7, v7
	v_fmac_f32_e32 v12, v167, v167
	v_pk_add_f32 v[164:165], v[24:25], v[92:93] op_sel_hi:[1,0] neg_lo:[0,1] neg_hi:[0,1]
	v_fmac_f32_e32 v12, v182, v182
	v_fmac_f32_e32 v12, v164, v164
	v_fmac_f32_e32 v12, v183, v183
	v_fmac_f32_e32 v12, v165, v165
	v_pk_add_f32 v[162:163], v[26:27], v[92:93] op_sel_hi:[1,0] neg_lo:[0,1] neg_hi:[0,1]
	v_fmac_f32_e32 v12, v180, v180
	v_fmac_f32_e32 v12, v162, v162
	v_fmac_f32_e32 v12, v181, v181
	v_fmac_f32_e32 v12, v163, v163
	v_pk_add_f32 v[160:161], v[28:29], v[92:93] op_sel_hi:[1,0] neg_lo:[0,1] neg_hi:[0,1]
	v_fmac_f32_e32 v12, v178, v178
	v_fmac_f32_e32 v12, v160, v160
	v_pk_add_f32 v[154:155], v[30:31], v[92:93] op_sel_hi:[1,0] neg_lo:[0,1] neg_hi:[0,1]
	v_pk_add_f32 v[176:177], v[14:15], v[92:93] op_sel_hi:[1,0] neg_lo:[0,1] neg_hi:[0,1]
	v_fmac_f32_e32 v12, v179, v179
	ds_read_b128 v[92:95], v253 offset:24896
	global_load_dwordx4 v[28:31], v[124:125], off offset:128
	global_load_dwordx4 v[20:23], v[124:125], off offset:160
	v_fmac_f32_e32 v12, v161, v161
	v_fmac_f32_e32 v12, v176, v176
	ds_read_b128 v[120:123], v253 offset:26944
	v_fmac_f32_e32 v12, v154, v154
	v_fmac_f32_e32 v12, v177, v177
	v_fmac_f32_e32 v12, v155, v155
	s_waitcnt vmcnt(14) lgkmcnt(5)
	v_mov_b32_e32 v13, v12
	s_nop 1
	v_permlane32_swap_b32_e32 v12, v13
	s_nop 0
	v_add_f32_e32 v12, v12, v13
	v_fmac_f32_e32 v126, 0x3c800000, v12
	v_mul_f32_e32 v12, 0x4f800000, v126
	v_cmp_gt_f32_e32 vcc, s8, v126
	s_nop 1
	v_cndmask_b32_e32 v12, v126, v12, vcc
	global_load_dwordx4 v[24:27], v[124:125], off offset:192
	global_load_dwordx4 v[16:19], v[124:125], off offset:224
	s_nop 0
	ds_read_b128 v[124:127], v253 offset:28992
	ds_read_b128 v[128:131], v253 offset:31040
	v_sqrt_f32_e32 v13, v12
	s_nop 0
	v_add_u32_e32 v14, -1, v13
	v_fma_f32 v15, -v14, v13, v12
	v_cmp_ge_f32_e64 s[2:3], 0, v15
	v_add_u32_e32 v15, 1, v13
	s_nop 0
	v_cndmask_b32_e64 v14, v13, v14, s[2:3]
	v_fma_f32 v13, -v15, v13, v12
	v_cmp_lt_f32_e64 s[2:3], 0, v13
	s_nop 1
	v_cndmask_b32_e64 v13, v14, v15, s[2:3]
	v_mul_f32_e32 v14, 0x37800000, v13
	s_mov_b32 s2, 0x8000
	v_cndmask_b32_e32 v13, v13, v14, vcc
	v_add_co_u32_e32 v188, vcc, s2, v156
	s_nop 1
	v_addc_co_u32_e32 v189, vcc, 0, v157, vcc
	v_cmp_class_f32_e32 vcc, v12, v208
	ds_read_b128 v[132:135], v253 offset:33088
	ds_read_b128 v[136:139], v253 offset:35456
	v_cndmask_b32_e32 v12, v13, v12, vcc
	v_div_scale_f32 v13, s[2:3], v12, v12, 1.0
	v_rcp_f32_e32 v14, v13
	s_mov_b32 s2, 0x9000
	s_mov_b32 s3, 0xbc90
	v_fma_f32 v15, -v13, v14, 1.0
	v_fmac_f32_e32 v14, v15, v14
	v_div_scale_f32 v15, vcc, 1.0, v12, 1.0
	v_mul_f32_e32 v82, v15, v14
	v_fma_f32 v190, -v13, v82, v15
	v_fmac_f32_e32 v82, v190, v14
	v_fma_f32 v13, -v13, v82, v15
	v_div_fmas_f32 v13, v13, v14, v82
	v_div_fixup_f32 v82, v13, v12, 1.0
	v_pk_mul_f32 v[190:191], v[6:7], v[82:83] op_sel_hi:[1,0]
	v_pk_mul_f32 v[192:193], v[4:5], v[82:83] op_sel_hi:[1,0]
	v_pk_mul_f32 v[4:5], v[8:9], v[82:83] op_sel_hi:[1,0]
	v_pk_mul_f32 v[6:7], v[10:11], v[82:83] op_sel_hi:[1,0]
	s_waitcnt vmcnt(7) lgkmcnt(9)
	v_pk_fma_f32 v[118:119], v[4:5], v[118:119], v[142:143]
	v_pk_fma_f32 v[116:117], v[6:7], v[116:117], v[140:141]
	s_waitcnt vmcnt(4) lgkmcnt(8)
	v_mfma_f32_32x32x16_f16 v[0:15], v[0:3], v[96:99], 0
	v_fma_f32 v72, v192, v72, v88
	v_fma_f32 v73, v193, v73, v89
	v_fma_f32 v74, v190, v74, v90
	v_fma_f32 v75, v191, v75, v91
	ds_read_b128 v[88:91], v253 offset:21824
	v_cvt_pk_f16_f32 v75, v74, v75
	v_cvt_pk_f16_f32 v74, v72, v73
	v_cvt_pk_f16_f32 v73, v118, v119
	v_pk_mul_f32 v[118:119], v[178:179], v[82:83] op_sel_hi:[1,0]
	s_waitcnt vmcnt(4) lgkmcnt(8)
	v_mfma_f32_32x32x16_f16 v[0:15], v[144:147], v[104:107], v[0:15]
	v_mul_f32_e64 v144, v180, v82
	v_mul_f32_e64 v145, v181, v82
	v_mul_f32_e64 v146, v182, v82
	v_mul_f32_e64 v147, v183, v82
	v_fma_f32 v144, v144, v78, v86
	v_fma_f32 v145, v145, v79, v87
	v_pk_fma_f32 v[146:147], v[146:147], v[76:77], v[84:85]
	ds_read_b128 v[84:87], v253 offset:23872
	v_add_co_u32_e32 v152, vcc, s2, v156
	s_waitcnt vmcnt(4) lgkmcnt(8)
	v_mfma_f32_32x32x16_f16 v[0:15], v[148:151], v[100:103], v[0:15]
	v_addc_co_u32_e32 v153, vcc, 0, v157, vcc
	v_fma_f32 v32, v118, v32, v68
	v_fma_f32 v33, v119, v33, v69
	v_cvt_pk_f16_f32 v69, v144, v145
	v_cvt_pk_f16_f32 v68, v146, v147
	ds_read_b128 v[144:147], v253 offset:27968
	ds_read_b128 v[148:151], v253 offset:32064
	s_waitcnt vmcnt(4) lgkmcnt(9)
	v_mfma_f32_32x32x16_f16 v[0:15], v[92:95], v[112:115], v[0:15]
	ds_read_b128 v[92:95], v253 offset:38528
	ds_read_b128 v[76:79], v253 offset:44672
	v_cvt_pk_f16_f32 v72, v116, v117
	v_mul_f32_e64 v116, v176, v82
	v_mul_f32_e64 v117, v177, v82
	v_pk_mul_f32 v[118:119], v[174:175], v[82:83] op_sel_hi:[1,0]
	v_pk_fma_f32 v[34:35], v[116:117], v[34:35], v[70:71]
	v_pk_mul_f32 v[116:117], v[172:173], v[82:83] op_sel_hi:[1,0]
	s_waitcnt vmcnt(2) lgkmcnt(10)
	v_mfma_f32_32x32x16_f16 v[0:15], v[120:123], v[108:111], v[0:15]
	ds_read_b128 v[120:123], v253 offset:30016
	v_fma_f32 v28, v118, v40, v28
	v_fma_f32 v29, v119, v41, v29
	v_fma_f32 v30, v116, v42, v30
	v_fma_f32 v31, v117, v43, v31
	v_cvt_pk_f16_f32 v40, v28, v29
	v_cvt_pk_f16_f32 v41, v30, v31
	v_pk_mul_f32 v[28:29], v[162:163], v[82:83] op_sel_hi:[1,0]
	v_pk_mul_f32 v[30:31], v[164:165], v[82:83] op_sel_hi:[1,0]
	s_waitcnt vmcnt(0) lgkmcnt(10)
	v_mfma_f32_32x32x16_f16 v[0:15], v[124:127], v[48:51], v[0:15]
	v_fma_f32 v24, v30, v36, v24
	v_fma_f32 v25, v31, v37, v25
	v_fma_f32 v26, v28, v38, v26
	v_fma_f32 v27, v29, v39, v27
	ds_read_b128 v[36:39], v253 offset:34112
	v_cvt_pk_f16_f32 v71, v34, v35
	v_cvt_pk_f16_f32 v70, v32, v33
	v_pk_mul_f32 v[32:33], v[166:167], v[82:83] op_sel_hi:[1,0]
	v_pk_mul_f32 v[34:35], v[168:169], v[82:83] op_sel_hi:[1,0]
	s_waitcnt vmcnt(0) lgkmcnt(10)
	v_mfma_f32_32x32x16_f16 v[0:15], v[128:131], v[52:55], v[0:15]
	ds_read_b128 v[126:129], v253 offset:25920
	v_fma_f32 v20, v34, v44, v20
	v_fma_f32 v21, v35, v45, v21
	v_fma_f32 v22, v32, v46, v22
	v_fma_f32 v23, v33, v47, v23
	v_cvt_pk_f16_f32 v42, v20, v21
	v_cvt_pk_f16_f32 v43, v22, v23
	v_pk_mul_f32 v[20:21], v[154:155], v[82:83] op_sel_hi:[1,0]
	v_pk_mul_f32 v[22:23], v[160:161], v[82:83] op_sel_hi:[1,0]
	s_waitcnt vmcnt(0) lgkmcnt(10)
	v_mfma_f32_32x32x16_f16 v[0:15], v[132:135], v[56:59], v[0:15]
	v_fma_f32 v16, v22, v64, v16
	v_fma_f32 v17, v23, v65, v17
	v_fma_f32 v18, v20, v66, v18
	v_fma_f32 v19, v21, v67, v19
	ds_read_b128 v[64:67], v253 offset:36480
	s_mov_b32 s2, 0xa714
	v_mov_b32_e32 v164, 0xb7d0
	v_cvt_pk_f16_f32 v34, v16, v17
	v_cvt_pk_f16_f32 v35, v18, v19
	s_waitcnt vmcnt(0) lgkmcnt(10)
	v_mfma_f32_32x32x16_f16 v[0:15], v[136:139], v[60:63], v[0:15]
	v_cvt_pk_f16_f32 v33, v26, v27
	v_cvt_pk_f16_f32 v32, v24, v25
	ds_read_b128 v[132:135], v253 offset:39552
	v_add_co_u32_e32 v136, vcc, s6, v156
	ds_read_b128 v[140:143], v253 offset:41600
	ds_read_b128 v[44:47], v253 offset:40576
	s_nop 5
	v_cvt_pk_f16_f32 v0, v0, v1
	v_and_b32_e32 v1, 0x7fff7fff, v0
	v_cvt_pk_f16_f32 v2, v2, v3
	v_pk_fma_f16 v16, v1, s2, v164 op_sel_hi:[1,0,0]
	v_and_b32_e32 v3, 0x7fff7fff, v2
	v_pk_fma_f16 v16, v16, v1, s3 op_sel_hi:[1,1,0]
	v_pk_fma_f16 v18, v3, s2, v164 op_sel_hi:[1,0,0]
	v_pk_mul_f16 v16, v1, v16
	v_pk_fma_f16 v18, v18, v3, s3 op_sel_hi:[1,1,0]
	v_exp_f16_e32 v17, v16
	v_exp_f16_sdwa v16, v16 dst_sel:DWORD dst_unused:UNUSED_PAD src0_sel:WORD_1
	v_pk_mul_f16 v18, v3, v18
	v_pk_add_f16 v0, v1, v0
	v_exp_f16_e32 v19, v18
	v_exp_f16_sdwa v18, v18 dst_sel:DWORD dst_unused:UNUSED_PAD src0_sel:WORD_1
	v_pack_b32_f16 v16, v17, v16
	v_pk_fma_f16 v116, v1, v16, v0 neg_lo:[1,0,0] neg_hi:[1,0,0]
	v_pk_add_f16 v1, v3, v2
	v_pack_b32_f16 v0, v19, v18
	v_pk_fma_f16 v117, v3, v0, v1 neg_lo:[1,0,0] neg_hi:[1,0,0]
	v_cvt_pk_f16_f32 v0, v4, v5
	v_and_b32_e32 v1, 0x7fff7fff, v0
	v_pk_fma_f16 v2, v1, s2, v164 op_sel_hi:[1,0,0]
	s_waitcnt vmcnt(0) lgkmcnt(8)
	v_mfma_f32_32x32x16_f16 v[16:31], v[92:95], v[96:99], 0
	v_pk_fma_f16 v2, v2, v1, s3 op_sel_hi:[1,1,0]
	v_cvt_pk_f16_f32 v4, v6, v7
	v_pk_mul_f16 v2, v1, v2
	v_and_b32_e32 v5, 0x7fff7fff, v4
	v_exp_f16_e32 v3, v2
	v_exp_f16_sdwa v2, v2 dst_sel:DWORD dst_unused:UNUSED_PAD src0_sel:WORD_1
	v_pk_fma_f16 v6, v5, s2, v164 op_sel_hi:[1,0,0]
	v_pk_add_f16 v0, v1, v0
	v_pk_fma_f16 v6, v6, v5, s3 op_sel_hi:[1,1,0]
	v_pack_b32_f16 v2, v3, v2
	v_pk_mul_f16 v6, v5, v6
	v_pk_fma_f16 v118, v1, v2, v0 neg_lo:[1,0,0] neg_hi:[1,0,0]
	v_cvt_pk_f16_f32 v1, v8, v9
	v_exp_f16_e32 v7, v6
	v_exp_f16_sdwa v6, v6 dst_sel:DWORD dst_unused:UNUSED_PAD src0_sel:WORD_1
	v_and_b32_e32 v2, 0x7fff7fff, v1
	v_pk_fma_f16 v3, v2, s2, v164 op_sel_hi:[1,0,0]
	v_mfma_f32_32x32x16_f16 v[16:31], v[88:91], v[104:107], v[16:31]
	v_pk_fma_f16 v3, v3, v2, s3 op_sel_hi:[1,1,0]
	v_pack_b32_f16 v0, v7, v6
	v_pk_mul_f16 v3, v2, v3
	v_pk_add_f16 v4, v5, v4
	v_exp_f16_e32 v6, v3
	v_exp_f16_sdwa v3, v3 dst_sel:DWORD dst_unused:UNUSED_PAD src0_sel:WORD_1
	v_pk_fma_f16 v119, v5, v0, v4 neg_lo:[1,0,0] neg_hi:[1,0,0]
	v_cvt_pk_f16_f32 v4, v10, v11
	v_pk_add_f16 v1, v2, v1
	v_pack_b32_f16 v0, v6, v3
	v_and_b32_e32 v5, 0x7fff7fff, v4
	v_pk_fma_f16 v124, v2, v0, v1 neg_lo:[1,0,0] neg_hi:[1,0,0]
	v_pk_fma_f16 v0, v5, s2, v164 op_sel_hi:[1,0,0]
	v_mfma_f32_32x32x16_f16 v[16:31], v[84:87], v[100:103], v[16:31]
	v_pk_fma_f16 v0, v0, v5, s3 op_sel_hi:[1,1,0]
	v_addc_co_u32_e32 v137, vcc, 0, v157, vcc
	v_pk_mul_f16 v0, v5, v0
	ds_read_b128 v[84:87], v253 offset:43648
	v_exp_f16_e32 v6, v0
	v_exp_f16_sdwa v7, v0 dst_sel:DWORD dst_unused:UNUSED_PAD src0_sel:WORD_1
	ds_read_b128 v[0:3], v254 offset:3072
	s_waitcnt vmcnt(0) lgkmcnt(6)
	v_mfma_f32_32x32x16_f16 v[16:31], v[126:129], v[112:115], v[16:31]
	s_mov_b32 s6, 0xb000
	v_cvt_pk_f16_f32 v8, v12, v13
	v_and_b32_e32 v9, 0x7fff7fff, v8
	v_pk_fma_f16 v10, v9, s2, v164 op_sel_hi:[1,0,0]
	v_pack_b32_f16 v6, v6, v7
	v_pk_fma_f16 v10, v10, v9, s3 op_sel_hi:[1,1,0]
	v_pk_add_f16 v4, v5, v4
	v_mfma_f32_32x32x16_f16 v[16:31], v[144:147], v[108:111], v[16:31]
	v_pk_mul_f16 v10, v9, v10
	v_pk_fma_f16 v125, v5, v6, v4 neg_lo:[1,0,0] neg_hi:[1,0,0]
	v_exp_f16_e32 v11, v10
	v_exp_f16_sdwa v10, v10 dst_sel:DWORD dst_unused:UNUSED_PAD src0_sel:WORD_1
	v_pk_add_f16 v5, v9, v8
	v_pack_b32_f16 v4, v11, v10
	v_mfma_f32_32x32x16_f16 v[16:31], v[120:123], v[48:51], v[16:31]
	v_pk_fma_f16 v126, v9, v4, v5 neg_lo:[1,0,0] neg_hi:[1,0,0]
	v_cvt_pk_f16_f32 v4, v14, v15
	v_and_b32_e32 v5, 0x7fff7fff, v4
	v_pk_fma_f16 v6, v5, s2, v164 op_sel_hi:[1,0,0]
	v_pk_add_f16 v4, v5, v4
	v_pk_fma_f16 v6, v6, v5, s3 op_sel_hi:[1,1,0]
	v_mfma_f32_32x32x16_f16 v[16:31], v[148:151], v[52:55], v[16:31]
	v_add_co_u32_e32 v150, vcc, s7, v156
	v_pk_mul_f16 v6, v5, v6
	s_nop 0
	v_addc_co_u32_e32 v151, vcc, 0, v157, vcc
	ds_read_b128 v[88:91], v253 offset:45696
	v_add_co_u32_e32 v152, vcc, s6, v156
	v_mfma_f32_32x32x16_f16 v[16:31], v[36:39], v[56:59], v[16:31]
	s_nop 0
	v_addc_co_u32_e32 v153, vcc, 0, v157, vcc
	ds_read_b128 v[92:95], v253 offset:47744
	ds_read_b128 v[146:149], v253 offset:48768
	ds_read_b128 v[120:123], v253 offset:51840
	ds_read_b128 v[166:169], v253 offset:50816
	v_exp_f16_e32 v7, v6
	s_waitcnt vmcnt(0) lgkmcnt(10)
	v_mfma_f32_32x32x16_f16 v[16:31], v[64:67], v[60:63], v[16:31]
	ds_read_b128 v[64:67], v253 offset:49792
	v_exp_f16_sdwa v6, v6 dst_sel:DWORD dst_unused:UNUSED_PAD src0_sel:WORD_1
	s_mov_b32 s6, 0xe000
	v_add_co_u32_e32 v138, vcc, s6, v156
	v_pack_b32_f16 v6, v7, v6
	v_pk_fma_f16 v127, v5, v6, v4 neg_lo:[1,0,0] neg_hi:[1,0,0]
	s_nop 5
	v_cvt_pk_f16_f32 v8, v16, v17
	v_and_b32_e32 v9, 0x7fff7fff, v8
	v_pk_fma_f16 v10, v9, s2, v164 op_sel_hi:[1,0,0]
	v_pk_add_f16 v5, v9, v8
	v_pk_fma_f16 v10, v10, v9, s3 op_sel_hi:[1,1,0]
	v_addc_co_u32_e32 v139, vcc, 0, v157, vcc
	v_pk_mul_f16 v10, v9, v10
	v_cvt_pk_f16_f32 v8, v20, v21
	v_exp_f16_e32 v11, v10
	v_exp_f16_sdwa v10, v10 dst_sel:DWORD dst_unused:UNUSED_PAD src0_sel:WORD_1
	v_and_b32_e32 v20, 0x7fff7fff, v8
	v_pk_add_f16 v82, v20, v8
	ds_read_b128 v[36:39], v254 offset:2048
	v_pack_b32_f16 v4, v11, v10
	v_pk_fma_f16 v128, v9, v4, v5 neg_lo:[1,0,0] neg_hi:[1,0,0]
	v_cvt_pk_f16_f32 v4, v18, v19
	ds_read_b128 v[16:19], v254 offset:1024
	v_and_b32_e32 v5, 0x7fff7fff, v4
	v_pk_fma_f16 v6, v5, s2, v164 op_sel_hi:[1,0,0]
	v_pk_fma_f16 v9, v20, s2, v164 op_sel_hi:[1,0,0]
	v_pk_fma_f16 v6, v6, v5, s3 op_sel_hi:[1,1,0]
	v_pk_fma_f16 v9, v9, v20, s3 op_sel_hi:[1,1,0]
	v_pk_mul_f16 v6, v5, v6
	v_pk_mul_f16 v9, v20, v9
	v_exp_f16_e32 v7, v6
	v_exp_f16_sdwa v6, v6 dst_sel:DWORD dst_unused:UNUSED_PAD src0_sel:WORD_1
	v_exp_f16_e32 v10, v9
	v_exp_f16_sdwa v9, v9 dst_sel:DWORD dst_unused:UNUSED_PAD src0_sel:WORD_1
	v_pk_add_f16 v4, v5, v4
	v_pack_b32_f16 v6, v7, v6
	v_pk_fma_f16 v129, v5, v6, v4 neg_lo:[1,0,0] neg_hi:[1,0,0]
	v_pack_b32_f16 v21, v10, v9
	s_waitcnt vmcnt(0) lgkmcnt(8)
	v_mfma_f32_32x32x16_f16 v[0:15], v[0:3], v[96:99], 0
	v_pk_fma_f16 v130, v20, v21, v82 neg_lo:[1,0,0] neg_hi:[1,0,0]
	v_cvt_pk_f16_f32 v82, v22, v23
	v_and_b32_e32 v131, 0x7fff7fff, v82
	v_pk_fma_f16 v20, v131, s2, v164 op_sel_hi:[1,0,0]
	v_cvt_pk_f16_f32 v24, v24, v25
	v_pk_fma_f16 v20, v20, v131, s3 op_sel_hi:[1,1,0]
	v_and_b32_e32 v25, 0x7fff7fff, v24
	v_pk_mul_f16 v20, v131, v20
	v_mfma_f32_32x32x16_f16 v[0:15], v[132:135], v[104:107], v[0:15]
	v_exp_f16_e32 v144, v20
	v_exp_f16_sdwa v132, v20 dst_sel:DWORD dst_unused:UNUSED_PAD src0_sel:WORD_1
	v_pk_fma_f16 v20, v25, s2, v164 op_sel_hi:[1,0,0]
	ds_read_b128 v[152:155], v253 offset:46720
	v_pk_fma_f16 v20, v20, v25, s3 op_sel_hi:[1,1,0]
	v_pack_b32_f16 v132, v144, v132
	v_pk_mul_f16 v133, v25, v20
	ds_read_b128 v[20:23], v254 offset:4096
	v_mfma_f32_32x32x16_f16 v[0:15], v[140:143], v[100:103], v[0:15]
	ds_read_b128 v[142:145], v253 offset:42624
	v_cvt_pk_f16_f32 v26, v26, v27
	v_and_b32_e32 v27, 0x7fff7fff, v26
	v_exp_f16_e32 v134, v133
	v_exp_f16_sdwa v133, v133 dst_sel:DWORD dst_unused:UNUSED_PAD src0_sel:WORD_1
	v_pk_add_f16 v82, v131, v82
	v_pk_add_f16 v24, v25, v24
	v_mfma_f32_32x32x16_f16 v[0:15], v[84:87], v[112:115], v[0:15]
	v_pk_fma_f16 v84, v27, s2, v164 op_sel_hi:[1,0,0]
	v_pk_fma_f16 v131, v131, v132, v82 neg_lo:[1,0,0] neg_hi:[1,0,0]
	v_pk_fma_f16 v84, v84, v27, s3 op_sel_hi:[1,1,0]
	v_pack_b32_f16 v82, v134, v133
	v_pk_mul_f16 v84, v27, v84
	v_pk_fma_f16 v132, v25, v82, v24 neg_lo:[1,0,0] neg_hi:[1,0,0]
	v_exp_f16_e32 v85, v84
	s_waitcnt vmcnt(0) lgkmcnt(10)
	v_mfma_f32_32x32x16_f16 v[0:15], v[88:91], v[108:111], v[0:15]
	v_exp_f16_sdwa v84, v84 dst_sel:DWORD dst_unused:UNUSED_PAD src0_sel:WORD_1
	v_pk_add_f16 v25, v27, v26
	ds_read_b128 v[170:173], v254
	s_mov_b32 s6, 0x13000
	v_pack_b32_f16 v24, v85, v84
	v_pk_fma_f16 v133, v27, v24, v25 neg_lo:[1,0,0] neg_hi:[1,0,0]
	v_cvt_pk_f16_f32 v24, v28, v29
	s_waitcnt vmcnt(0) lgkmcnt(10)
	v_mfma_f32_32x32x16_f16 v[0:15], v[92:95], v[72:75], v[0:15]
	v_and_b32_e32 v25, 0x7fff7fff, v24
	v_cvt_pk_f16_f32 v28, v30, v31
	v_pk_fma_f16 v26, v25, s2, v164 op_sel_hi:[1,0,0]
	v_and_b32_e32 v29, 0x7fff7fff, v28
	v_pk_fma_f16 v26, v26, v25, s3 op_sel_hi:[1,1,0]
	v_pk_fma_f16 v30, v29, s2, v164 op_sel_hi:[1,0,0]
	v_pk_mul_f16 v26, v25, v26
	s_waitcnt vmcnt(0) lgkmcnt(6)
	v_mfma_f32_32x32x16_f16 v[0:15], v[64:67], v[68:71], v[0:15]
	v_pk_fma_f16 v30, v30, v29, s3 op_sel_hi:[1,1,0]
	v_exp_f16_e32 v27, v26
	v_exp_f16_sdwa v26, v26 dst_sel:DWORD dst_unused:UNUSED_PAD src0_sel:WORD_1
	v_pk_mul_f16 v30, v29, v30
	v_pk_add_f16 v24, v25, v24
	v_exp_f16_e32 v31, v30
	v_exp_f16_sdwa v30, v30 dst_sel:DWORD dst_unused:UNUSED_PAD src0_sel:WORD_1
	v_mfma_f32_32x32x16_f16 v[0:15], v[120:123], v[40:43], v[0:15]
	v_pack_b32_f16 v26, v27, v26
	v_pk_fma_f16 v134, v25, v26, v24 neg_lo:[1,0,0] neg_hi:[1,0,0]
	v_pack_b32_f16 v24, v31, v30
	v_pk_add_f16 v25, v29, v28
	v_add_co_u32_e32 v150, vcc, s6, v156
	v_pk_fma_f16 v135, v29, v24, v25 neg_lo:[1,0,0] neg_hi:[1,0,0]
	s_waitcnt vmcnt(0) lgkmcnt(4)
	v_mfma_f32_32x32x16_f16 v[0:15], v[16:19], v[32:35], v[0:15]
	v_addc_co_u32_e32 v151, vcc, 0, v157, vcc
	ds_read_b128 v[64:67], v254 offset:5120
	ds_read_b128 v[84:87], v254 offset:7168
	s_mov_b32 s6, 0x10000
	v_add_co_u32_e32 v140, vcc, s6, v156
	s_nop 6
	v_cvt_pk_f16_f32 v16, v0, v1
	v_and_b32_e32 v17, 0x7fff7fff, v16
	v_pk_fma_f16 v0, v17, s2, v164 op_sel_hi:[1,0,0]
	v_cvt_pk_f16_f32 v24, v2, v3
	v_pk_fma_f16 v0, v0, v17, s3 op_sel_hi:[1,1,0]
	v_and_b32_e32 v25, 0x7fff7fff, v24
	v_pk_mul_f16 v0, v17, v0
	v_pk_add_f16 v16, v17, v16
	v_exp_f16_e32 v18, v0
	v_exp_f16_sdwa v19, v0 dst_sel:DWORD dst_unused:UNUSED_PAD src0_sel:WORD_1
	v_pk_fma_f16 v0, v25, s2, v164 op_sel_hi:[1,0,0]
	v_addc_co_u32_e32 v141, vcc, 0, v157, vcc
	v_pk_fma_f16 v0, v0, v25, s3 op_sel_hi:[1,1,0]
	v_pack_b32_f16 v18, v18, v19
	v_pk_mul_f16 v26, v25, v0
	ds_read_b128 v[0:3], v254 offset:21824
	v_exp_f16_e32 v27, v26
	v_exp_f16_sdwa v26, v26 dst_sel:DWORD dst_unused:UNUSED_PAD src0_sel:WORD_1
	v_pk_fma_f16 v120, v17, v18, v16 neg_lo:[1,0,0] neg_hi:[1,0,0]
	v_pk_add_f16 v17, v25, v24
	ds_read_b128 v[88:91], v254 offset:9216
	v_pack_b32_f16 v16, v27, v26
	v_pk_fma_f16 v121, v25, v16, v17 neg_lo:[1,0,0] neg_hi:[1,0,0]
	s_waitcnt vmcnt(0) lgkmcnt(6)
	v_mfma_f32_32x32x16_f16 v[16:31], v[20:23], v[96:99], 0
	v_cvt_pk_f16_f32 v82, v4, v5
	s_mov_b32 s6, 0xf000
	v_and_b32_e32 v122, 0x7fff7fff, v82
	v_add_co_u32_e32 v162, vcc, s6, v156
	v_pk_fma_f16 v4, v122, s2, v164 op_sel_hi:[1,0,0]
	s_nop 0
	v_addc_co_u32_e32 v163, vcc, 0, v157, vcc
	v_mfma_f32_32x32x16_f16 v[16:31], v[44:47], v[104:107], v[16:31]
	v_pk_fma_f16 v4, v4, v122, s3 op_sel_hi:[1,1,0]
	ds_read_b128 v[92:95], v254 offset:11264
	v_pk_mul_f16 v4, v122, v4
	v_cvt_pk_f16_f32 v45, v6, v7
	v_exp_f16_e32 v5, v4
	v_exp_f16_sdwa v4, v4 dst_sel:DWORD dst_unused:UNUSED_PAD src0_sel:WORD_1
	v_and_b32_e32 v46, 0x7fff7fff, v45
	s_waitcnt vmcnt(0) lgkmcnt(6)
	v_mfma_f32_32x32x16_f16 v[16:31], v[142:145], v[100:103], v[16:31]
	s_mov_b32 s6, 0x11000
	v_pack_b32_f16 v44, v5, v4
	v_pk_fma_f16 v4, v46, s2, v164 op_sel_hi:[1,0,0]
	v_cvt_pk_f16_f32 v10, v10, v11
	v_pk_fma_f16 v4, v4, v46, s3 op_sel_hi:[1,1,0]
	v_and_b32_e32 v11, 0x7fff7fff, v10
	v_pk_mul_f16 v47, v46, v4
	v_mfma_f32_32x32x16_f16 v[16:31], v[76:79], v[112:115], v[16:31]
	ds_read_b128 v[4:7], v254 offset:13312
	v_exp_f16_e32 v76, v47
	v_exp_f16_sdwa v47, v47 dst_sel:DWORD dst_unused:UNUSED_PAD src0_sel:WORD_1
	v_pk_add_f16 v77, v122, v82
	v_pk_add_f16 v45, v46, v45
	v_pk_fma_f16 v122, v122, v44, v77 neg_lo:[1,0,0] neg_hi:[1,0,0]
	v_pack_b32_f16 v44, v76, v47
	v_mfma_f32_32x32x16_f16 v[16:31], v[152:155], v[108:111], v[16:31]
	ds_read_b128 v[76:79], v254 offset:15360
	v_cvt_pk_f16_f32 v47, v8, v9
	v_add_co_u32_e32 v8, vcc, s6, v156
	v_and_b32_e32 v82, 0x7fff7fff, v47
	s_nop 0
	v_addc_co_u32_e32 v9, vcc, 0, v157, vcc
	v_mfma_f32_32x32x16_f16 v[16:31], v[146:149], v[72:75], v[16:31]
	ds_read_b128 v[72:75], v254 offset:17728
	v_pk_fma_f16 v123, v82, s2, v164 op_sel_hi:[1,0,0]
	s_mov_b32 s6, 0x12000
	v_pk_fma_f16 v123, v123, v82, s3 op_sel_hi:[1,1,0]
	v_add_co_u32_e32 v160, vcc, s6, v156
	ds_read_b128 v[146:149], v254 offset:6144
	v_mfma_f32_32x32x16_f16 v[16:31], v[166:169], v[68:71], v[16:31]
	v_pk_mul_f16 v68, v82, v123
	v_addc_co_u32_e32 v161, vcc, 0, v157, vcc
	v_exp_f16_e32 v136, v68
	v_exp_f16_sdwa v137, v68 dst_sel:DWORD dst_unused:UNUSED_PAD src0_sel:WORD_1
	ds_read_b128 v[68:71], v254 offset:19776
	ds_read_b128 v[142:145], v254 offset:22848
	s_waitcnt vmcnt(0) lgkmcnt(11)
	v_mfma_f32_32x32x16_f16 v[16:31], v[170:173], v[40:43], v[16:31]
	v_pk_fma_f16 v123, v46, v44, v45 neg_lo:[1,0,0] neg_hi:[1,0,0]
	v_pack_b32_f16 v136, v136, v137
	v_pk_add_f16 v137, v82, v47
	ds_read_b128 v[170:173], v254 offset:16384
	v_pk_fma_f16 v136, v82, v136, v137 neg_lo:[1,0,0] neg_hi:[1,0,0]
	s_mov_b32 s6, 0x16000
	ds_read_b128 v[152:155], v254 offset:25920
	v_mfma_f32_32x32x16_f16 v[16:31], v[36:39], v[32:35], v[16:31]
	v_pk_fma_f16 v32, v11, s2, v164 op_sel_hi:[1,0,0]
	s_nop 0
	v_pk_fma_f16 v32, v32, v11, s3 op_sel_hi:[1,1,0]
	s_nop 0
	v_pk_mul_f16 v32, v11, v32
	s_nop 6
	v_cvt_pk_f16_f32 v24, v24, v25
	v_exp_f16_e32 v165, v32
	v_exp_f16_sdwa v166, v32 dst_sel:DWORD dst_unused:UNUSED_PAD src0_sel:WORD_1
	s_waitcnt vmcnt(0) lgkmcnt(10)
	v_mfma_f32_32x32x16_f16 v[32:47], v[0:3], v[96:99], 0
	v_pk_add_f16 v1, v11, v10
	v_cvt_pk_f16_f32 v10, v14, v15
	v_pack_b32_f16 v0, v165, v166
	ds_read_b128 v[166:169], v254 offset:8192
	v_pk_fma_f16 v137, v11, v0, v1 neg_lo:[1,0,0] neg_hi:[1,0,0]
	v_cvt_pk_f16_f32 v0, v12, v13
	v_and_b32_e32 v1, 0x7fff7fff, v0
	v_mfma_f32_32x32x16_f16 v[32:47], v[64:67], v[104:107], v[32:47]
	ds_read_b128 v[64:67], v254 offset:10240
	v_pk_fma_f16 v2, v1, s2, v164 op_sel_hi:[1,0,0]
	v_and_b32_e32 v11, 0x7fff7fff, v10
	v_pk_fma_f16 v2, v2, v1, s3 op_sel_hi:[1,1,0]
	v_pk_fma_f16 v12, v11, s2, v164 op_sel_hi:[1,0,0]
	v_pk_mul_f16 v2, v1, v2
	v_pk_fma_f16 v12, v12, v11, s3 op_sel_hi:[1,1,0]
	v_mfma_f32_32x32x16_f16 v[32:47], v[84:87], v[100:103], v[32:47]
	v_exp_f16_e32 v3, v2
	v_exp_f16_sdwa v2, v2 dst_sel:DWORD dst_unused:UNUSED_PAD src0_sel:WORD_1
	v_pk_mul_f16 v12, v11, v12
	v_pk_add_f16 v0, v1, v0
	v_exp_f16_e32 v13, v12
	v_exp_f16_sdwa v12, v12 dst_sel:DWORD dst_unused:UNUSED_PAD src0_sel:WORD_1
	v_pack_b32_f16 v2, v3, v2
	s_waitcnt vmcnt(0) lgkmcnt(11)
	v_mfma_f32_32x32x16_f16 v[32:47], v[88:91], v[112:115], v[32:47]
	ds_read_b128 v[88:91], v254 offset:12288
	v_pk_fma_f16 v138, v1, v2, v0 neg_lo:[1,0,0] neg_hi:[1,0,0]
	v_pack_b32_f16 v0, v13, v12
	v_pk_add_f16 v1, v11, v10
	v_add_co_u32_e32 v162, vcc, s6, v156
	v_pk_fma_f16 v139, v11, v0, v1 neg_lo:[1,0,0] neg_hi:[1,0,0]
	s_waitcnt vmcnt(0) lgkmcnt(11)
	v_mfma_f32_32x32x16_f16 v[32:47], v[92:95], v[108:111], v[32:47]
	ds_read_b128 v[92:95], v254 offset:14336
	v_cvt_pk_f16_f32 v0, v16, v17
	v_and_b32_e32 v1, 0x7fff7fff, v0
	v_pk_fma_f16 v2, v1, s2, v164 op_sel_hi:[1,0,0]
	v_pk_add_f16 v0, v1, v0
	v_pk_fma_f16 v2, v2, v1, s3 op_sel_hi:[1,1,0]
	v_addc_co_u32_e32 v163, vcc, 0, v157, vcc
	s_waitcnt vmcnt(0) lgkmcnt(11)
	v_mfma_f32_32x32x16_f16 v[32:47], v[4:7], v[48:51], v[32:47]
	v_cvt_pk_f16_f32 v4, v18, v19
	v_and_b32_e32 v5, 0x7fff7fff, v4
	ds_read_b128 v[16:19], v254 offset:18752
	v_pk_fma_f16 v6, v5, s2, v164 op_sel_hi:[1,0,0]
	v_pk_mul_f16 v2, v1, v2
	v_pk_fma_f16 v6, v6, v5, s3 op_sel_hi:[1,1,0]
	v_exp_f16_e32 v3, v2
	s_waitcnt vmcnt(0) lgkmcnt(11)
	v_mfma_f32_32x32x16_f16 v[32:47], v[76:79], v[52:55], v[32:47]
	v_exp_f16_sdwa v2, v2 dst_sel:DWORD dst_unused:UNUSED_PAD src0_sel:WORD_1
	v_pk_mul_f16 v6, v5, v6
	ds_read_b128 v[84:87], v254 offset:28992
	v_exp_f16_e32 v7, v6
	v_exp_f16_sdwa v6, v6 dst_sel:DWORD dst_unused:UNUSED_PAD src0_sel:WORD_1
	v_pack_b32_f16 v2, v3, v2
	v_pk_fma_f16 v140, v1, v2, v0 neg_lo:[1,0,0] neg_hi:[1,0,0]
	s_waitcnt vmcnt(0) lgkmcnt(11)
	v_mfma_f32_32x32x16_f16 v[32:47], v[72:75], v[56:59], v[32:47]
	v_pack_b32_f16 v0, v7, v6
	ds_read_b128 v[72:75], v254 offset:20800
	v_pk_add_f16 v1, v5, v4
	s_mov_b32 s6, 0x14000
	v_pk_fma_f16 v141, v5, v0, v1 neg_lo:[1,0,0] neg_hi:[1,0,0]
	v_lshlrev_b32_e32 v0, 2, v159
	v_ashrrev_i32_e32 v1, 31, v0
	v_lshl_add_u64 v[0:1], v[0:1], 2, v[80:81]
	global_load_dwordx4 v[76:79], v[0:1], off
	s_waitcnt vmcnt(1) lgkmcnt(10)
	v_mfma_f32_32x32x16_f16 v[32:47], v[68:71], v[60:63], v[32:47]
	ds_read_b128 v[68:71], v254 offset:40576
	ds_read_b128 v[174:177], v254 offset:23872
	s_waitcnt vmcnt(0) lgkmcnt(2)
	v_cvt_pk_f16_f32 v79, v20, v21
	v_and_b32_e32 v80, 0x7fff7fff, v79
	v_pk_fma_f16 v20, v80, s2, v164 op_sel_hi:[1,0,0]
	v_pk_add_f16 v79, v80, v79
	v_pk_fma_f16 v20, v20, v80, s3 op_sel_hi:[1,1,0]
	v_and_b32_e32 v25, 0x7fff7fff, v24
	v_mfma_f32_32x32x16_f16 v[0:15], v[142:145], v[96:99], 0
	v_cvt_pk_f16_f32 v143, v22, v23
	v_pk_mul_f16 v20, v80, v20
	v_and_b32_e32 v144, 0x7fff7fff, v143
	v_exp_f16_e32 v81, v20
	v_exp_f16_sdwa v82, v20 dst_sel:DWORD dst_unused:UNUSED_PAD src0_sel:WORD_1
	v_pk_fma_f16 v20, v144, s2, v164 op_sel_hi:[1,0,0]
	v_cvt_pk_f16_f32 v26, v26, v27
	v_pk_fma_f16 v20, v20, v144, s3 op_sel_hi:[1,1,0]
	v_mfma_f32_32x32x16_f16 v[0:15], v[146:149], v[104:107], v[0:15]
	v_pk_mul_f16 v142, v144, v20
	ds_read_b128 v[20:23], v254 offset:27968
	v_add_co_u32_e32 v148, vcc, s6, v156
	s_mov_b32 s6, 0x15000
	s_nop 0
	v_addc_co_u32_e32 v149, vcc, 0, v157, vcc
	v_mfma_f32_32x32x16_f16 v[0:15], v[166:169], v[100:103], v[0:15]
	ds_read_b128 v[166:169], v254 offset:32064
	ds_read_b128 v[178:181], v254 offset:24896
	v_add_co_u32_e32 v194, vcc, s6, v156
	v_exp_f16_e32 v145, v142
	s_nop 0
	v_addc_co_u32_e32 v195, vcc, 0, v157, vcc
	v_exp_f16_sdwa v146, v142 dst_sel:DWORD dst_unused:UNUSED_PAD src0_sel:WORD_1
	v_mfma_f32_32x32x16_f16 v[0:15], v[64:67], v[112:115], v[0:15]
	ds_read_b128 v[64:67], v254 offset:36480
	v_pack_b32_f16 v81, v81, v82
	v_pk_fma_f16 v142, v80, v81, v79 neg_lo:[1,0,0] neg_hi:[1,0,0]
	v_pack_b32_f16 v79, v145, v146
	v_pk_add_f16 v80, v144, v143
	s_mov_b32 s6, 0x18000
	v_pk_fma_f16 v143, v144, v79, v80 neg_lo:[1,0,0] neg_hi:[1,0,0]
	v_mfma_f32_32x32x16_f16 v[0:15], v[88:91], v[108:111], v[0:15]
	ds_read_b128 v[88:91], v254 offset:41600
	v_pk_fma_f16 v79, v25, s2, v164 op_sel_hi:[1,0,0]
	v_add_co_u32_e32 v160, vcc, s6, v156
	v_pk_fma_f16 v79, v79, v25, s3 op_sel_hi:[1,1,0]
	v_pk_add_f16 v24, v25, v24
	v_pk_mul_f16 v79, v25, v79
	v_mfma_f32_32x32x16_f16 v[0:15], v[92:95], v[48:51], v[0:15]
	ds_read_b128 v[92:95], v254 offset:33088
	ds_read_b128 v[186:189], v254 offset:31040
	v_exp_f16_e32 v48, v79
	v_exp_f16_sdwa v49, v79 dst_sel:DWORD dst_unused:UNUSED_PAD src0_sel:WORD_1
	v_addc_co_u32_e32 v161, vcc, 0, v157, vcc
	v_and_b32_e32 v27, 0x7fff7fff, v26
	v_mfma_f32_32x32x16_f16 v[0:15], v[170:173], v[52:55], v[0:15]
	v_pack_b32_f16 v48, v48, v49
	v_pk_fma_f16 v144, v25, v48, v24 neg_lo:[1,0,0] neg_hi:[1,0,0]
	v_cvt_pk_f16_f32 v25, v28, v29
	v_pk_fma_f16 v50, v27, s2, v164 op_sel_hi:[1,0,0]
	v_mov_b32_e32 v82, v83
	v_pk_fma_f16 v50, v50, v27, s3 op_sel_hi:[1,1,0]
	ds_read_b128 v[170:173], v254 offset:30016
	v_mfma_f32_32x32x16_f16 v[0:15], v[16:19], v[56:59], v[0:15]
	v_pk_mul_f16 v50, v27, v50
	ds_read_b128 v[182:185], v254 offset:34112
	v_exp_f16_e32 v51, v50
	v_exp_f16_sdwa v50, v50 dst_sel:DWORD dst_unused:UNUSED_PAD src0_sel:WORD_1
	v_and_b32_e32 v16, 0x7fff7fff, v25
	v_pk_fma_f16 v17, v16, s2, v164 op_sel_hi:[1,0,0]
	s_mov_b32 s6, 0x17000
	v_mfma_f32_32x32x16_f16 v[0:15], v[72:75], v[60:63], v[0:15]
	ds_read_b128 v[72:75], v254 offset:37504
	v_pack_b32_f16 v24, v51, v50
	v_cvt_pk_f16_f32 v19, v76, v77
	v_cvt_pk_f16_f32 v28, v78, 1.0
	ds_read_b128 v[76:79], v254 offset:42624
	v_cndmask_b32_e64 v80, 0, v19, s[4:5]
	v_cndmask_b32_e64 v81, 0, v28, s[4:5]
	v_pk_fma_f16 v17, v17, v16, s3 op_sel_hi:[1,1,0]
	v_add_co_u32_e32 v202, vcc, s6, v156
	s_waitcnt vmcnt(0) lgkmcnt(12)
	v_mfma_f32_32x32x16_f16 v[48:63], v[68:71], v[80:83], 0
	v_pk_mul_f16 v17, v16, v17
	v_addc_co_u32_e32 v203, vcc, 0, v157, vcc
	v_exp_f16_e32 v18, v17
	v_exp_f16_sdwa v17, v17 dst_sel:DWORD dst_unused:UNUSED_PAD src0_sel:WORD_1
	ds_read_b128 v[190:193], v254 offset:43648
	v_pk_add_f16 v19, v27, v26
	s_waitcnt vmcnt(0) lgkmcnt(12)
	v_mfma_f32_32x32x16_f16 v[48:63], v[174:177], v[116:119], v[48:63]
	v_pk_fma_f16 v145, v27, v24, v19 neg_lo:[1,0,0] neg_hi:[1,0,0]
	v_pack_b32_f16 v17, v18, v17
	v_pk_add_f16 v18, v16, v25
	v_cvt_pk_f16_f32 v19, v30, v31
	v_and_b32_e32 v24, 0x7fff7fff, v19
	v_pk_fma_f16 v146, v16, v17, v18 neg_lo:[1,0,0] neg_hi:[1,0,0]
	v_cvt_pk_f16_f32 v17, v32, v33
	s_waitcnt vmcnt(0) lgkmcnt(11)
	v_mfma_f32_32x32x16_f16 v[48:63], v[20:23], v[124:127], v[48:63]
	v_pk_fma_f16 v25, v24, s2, v164 op_sel_hi:[1,0,0]
	v_and_b32_e32 v32, 0x7fff7fff, v17
	v_pk_fma_f16 v25, v25, v24, s3 op_sel_hi:[1,1,0]
	v_pk_fma_f16 v18, v32, s2, v164 op_sel_hi:[1,0,0]
	v_pk_mul_f16 v25, v24, v25
	v_pk_fma_f16 v18, v18, v32, s3 op_sel_hi:[1,1,0]
	v_exp_f16_e32 v26, v25
	s_waitcnt vmcnt(0) lgkmcnt(10)
	v_mfma_f32_32x32x16_f16 v[48:63], v[166:169], v[128:131], v[48:63]
	ds_read_b128 v[166:169], v254 offset:38528
	v_exp_f16_sdwa v25, v25 dst_sel:DWORD dst_unused:UNUSED_PAD src0_sel:WORD_1
	ds_read_b128 v[174:177], v254 offset:26944
	v_pk_mul_f16 v18, v32, v18
	v_pk_add_f16 v19, v24, v19
	v_exp_f16_e32 v20, v18
	v_exp_f16_sdwa v18, v18 dst_sel:DWORD dst_unused:UNUSED_PAD src0_sel:WORD_1
	v_pack_b32_f16 v16, v26, v25
	v_pk_fma_f16 v147, v24, v16, v19 neg_lo:[1,0,0] neg_hi:[1,0,0]
	s_waitcnt vmcnt(0) lgkmcnt(10)
	v_mfma_f32_32x32x16_f16 v[48:63], v[64:67], v[132:135], v[48:63]
	v_pack_b32_f16 v33, v20, v18
	v_pk_add_f16 v64, v32, v17
	v_cvt_pk_f16_f32 v36, v36, v37
	v_pk_fma_f16 v148, v32, v33, v64 neg_lo:[1,0,0] neg_hi:[1,0,0]
	v_cvt_pk_f16_f32 v32, v34, v35
	v_and_b32_e32 v33, 0x7fff7fff, v32
	v_pk_fma_f16 v34, v33, s2, v164 op_sel_hi:[1,0,0]
	s_waitcnt vmcnt(0) lgkmcnt(9)
	v_mfma_f32_32x32x16_f16 v[16:31], v[88:91], v[80:83], 0
	v_pk_fma_f16 v34, v34, v33, s3 op_sel_hi:[1,1,0]
	v_and_b32_e32 v37, 0x7fff7fff, v36
	v_pk_mul_f16 v34, v33, v34
	v_pk_add_f16 v32, v33, v32
	v_exp_f16_e32 v35, v34
	v_exp_f16_sdwa v34, v34 dst_sel:DWORD dst_unused:UNUSED_PAD src0_sel:WORD_1
	v_pk_fma_f16 v64, v37, s2, v164 op_sel_hi:[1,0,0]
	v_mfma_f32_32x32x16_f16 v[16:31], v[178:181], v[116:119], v[16:31]
	v_pk_fma_f16 v64, v64, v37, s3 op_sel_hi:[1,1,0]
	v_pack_b32_f16 v34, v35, v34
	v_pk_fma_f16 v149, v33, v34, v32 neg_lo:[1,0,0] neg_hi:[1,0,0]
	ds_read_b128 v[32:35], v254 offset:35456
	v_pk_mul_f16 v64, v37, v64
	v_pk_add_f16 v36, v37, v36
	v_exp_f16_e32 v65, v64
	v_exp_f16_sdwa v64, v64 dst_sel:DWORD dst_unused:UNUSED_PAD src0_sel:WORD_1
	v_mfma_f32_32x32x16_f16 v[16:31], v[84:87], v[124:127], v[16:31]
	v_cvt_pk_f16_f32 v84, v38, v39
	v_and_b32_e32 v85, 0x7fff7fff, v84
	v_pack_b32_f16 v64, v65, v64
	v_pk_fma_f16 v150, v37, v64, v36 neg_lo:[1,0,0] neg_hi:[1,0,0]
	v_pk_fma_f16 v36, v85, s2, v164 op_sel_hi:[1,0,0]
	s_mov_b32 s6, 0x1b000
	v_pk_fma_f16 v64, v36, v85, s3 op_sel_hi:[1,1,0]
	ds_read_b128 v[36:39], v254 offset:39552
	s_waitcnt vmcnt(0) lgkmcnt(10)
	v_mfma_f32_32x32x16_f16 v[16:31], v[92:95], v[128:131], v[16:31]
	v_add_co_u32_e32 v204, vcc, s6, v156
	v_pk_mul_f16 v86, v85, v64
	s_nop 0
	v_addc_co_u32_e32 v205, vcc, 0, v157, vcc
	ds_read_b128 v[178:181], v255 offset:8192
	ds_read_b128 v[194:197], v254 offset:46720
	ds_read_b128 v[198:201], v254 offset:44672
	s_waitcnt vmcnt(0) lgkmcnt(9)
	v_mfma_f32_32x32x16_f16 v[16:31], v[72:75], v[132:135], v[16:31]
	v_cvt_pk_f16_f32 v40, v40, v41
	v_and_b32_e32 v41, 0x7fff7fff, v40
	v_pk_fma_f16 v88, v41, s2, v164 op_sel_hi:[1,0,0]
	v_exp_f16_e32 v87, v86
	v_pk_fma_f16 v88, v88, v41, s3 op_sel_hi:[1,1,0]
	v_exp_f16_sdwa v86, v86 dst_sel:DWORD dst_unused:UNUSED_PAD src0_sel:WORD_1
	v_pk_mul_f16 v88, v41, v88
	s_waitcnt vmcnt(0) lgkmcnt(8)
	v_mfma_f32_32x32x16_f16 v[64:79], v[76:79], v[80:83], 0
	v_exp_f16_e32 v89, v88
	v_exp_f16_sdwa v88, v88 dst_sel:DWORD dst_unused:UNUSED_PAD src0_sel:WORD_1
	v_pack_b32_f16 v86, v87, v86
	v_pk_add_f16 v84, v85, v84
	v_pk_add_f16 v40, v41, v40
	v_pk_fma_f16 v151, v85, v86, v84 neg_lo:[1,0,0] neg_hi:[1,0,0]
	v_pack_b32_f16 v84, v89, v88
	v_mfma_f32_32x32x16_f16 v[64:79], v[152:155], v[116:119], v[64:79]
	v_pk_fma_f16 v152, v41, v84, v40 neg_lo:[1,0,0] neg_hi:[1,0,0]
	v_cvt_pk_f16_f32 v153, v42, v43
	ds_read_b128 v[40:43], v254 offset:48768
	s_mov_b32 s6, 0x1a000
	v_add_co_u32_e32 v154, vcc, s6, v156
	s_mov_b32 s6, 0x19000
	v_mfma_f32_32x32x16_f16 v[64:79], v[170:173], v[124:127], v[64:79]
	v_addc_co_u32_e32 v155, vcc, 0, v157, vcc
	ds_read_b128 v[170:173], v254 offset:50816
	v_add_co_u32_e32 v162, vcc, s6, v156
	v_and_b32_e32 v159, 0x7fff7fff, v153
	s_nop 0
	v_addc_co_u32_e32 v163, vcc, 0, v157, vcc
	v_mfma_f32_32x32x16_f16 v[64:79], v[182:185], v[128:131], v[64:79]
	v_pk_fma_f16 v84, v159, s2, v164 op_sel_hi:[1,0,0]
	ds_read_b128 v[182:185], v255 offset:2048
	v_pk_fma_f16 v84, v84, v159, s3 op_sel_hi:[1,1,0]
	s_mov_b32 s6, 0x1c000
	v_pk_mul_f16 v84, v159, v84
	v_cvt_pk_f16_f32 v48, v48, v49
	v_exp_f16_e32 v165, v84
	s_waitcnt vmcnt(0) lgkmcnt(9)
	v_mfma_f32_32x32x16_f16 v[64:79], v[166:169], v[132:135], v[64:79]
	ds_read_b128 v[166:169], v255
	v_exp_f16_sdwa v206, v84 dst_sel:DWORD dst_unused:UNUSED_PAD src0_sel:WORD_1
	v_cvt_pk_f16_f32 v49, v50, v51
	v_cvt_pk_f16_f32 v50, v52, v53
	v_cvt_pk_f16_f32 v51, v54, v55
	v_cvt_pk_f16_f32 v24, v24, v25
	v_cvt_pk_f16_f32 v25, v26, v27
	v_mfma_f32_32x32x16_f16 v[80:95], v[190:193], v[80:83], 0
	v_cvt_pk_f16_f32 v26, v28, v29
	v_cvt_pk_f16_f32 v27, v30, v31
	ds_read_b128 v[28:31], v254 offset:49792
	v_cvt_pk_f16_f32 v20, v20, v21
	v_cvt_pk_f16_f32 v21, v22, v23
	v_pk_max_f16 v23, v21, 0
	v_pk_max_f16 v22, v20, 0
	s_waitcnt vmcnt(0) lgkmcnt(10)
	v_mfma_f32_32x32x16_f16 v[80:95], v[174:177], v[116:119], v[80:95]
	ds_read_b128 v[116:119], v255 offset:4096
	v_pk_max_f16 v176, v50, 0
	v_pk_max_f16 v175, v49, 0
	v_pk_max_f16 v174, v48, 0
	v_cvt_pk_f16_f32 v48, v56, v57
	v_cvt_pk_f16_f32 v49, v58, v59
	v_cvt_pk_f16_f32 v50, v60, v61
	v_mfma_f32_32x32x16_f16 v[80:95], v[186:189], v[124:127], v[80:95]
	v_add_co_u32_e32 v186, vcc, s6, v156
	v_pk_max_f16 v177, v51, 0
	s_nop 0
	v_addc_co_u32_e32 v187, vcc, 0, v157, vcc
	ds_read_b128 v[124:127], v255 offset:6144
	v_pk_max_f16 v27, v27, 0
	s_waitcnt vmcnt(0) lgkmcnt(11)
	v_mfma_f32_32x32x16_f16 v[80:95], v[32:35], v[128:131], v[80:95]
	v_cvt_pk_f16_f32 v32, v62, v63
	v_pk_max_f16 v131, v32, 0
	ds_read_b128 v[32:35], v255 offset:9216
	v_pk_max_f16 v130, v50, 0
	v_pk_max_f16 v129, v49, 0
	v_pk_max_f16 v128, v48, 0
	v_pk_max_f16 v26, v26, 0
	s_waitcnt vmcnt(0) lgkmcnt(11)
	v_mfma_f32_32x32x16_f16 v[80:95], v[36:39], v[132:135], v[80:95]
	v_cvt_pk_f16_f32 v36, v16, v17
	v_cvt_pk_f16_f32 v37, v18, v19
	ds_read_b128 v[16:19], v254 offset:45696
	ds_read_b128 v[132:135], v254 offset:47744
	v_cvt_pk_f16_f32 v38, v68, v69
	v_cvt_pk_f16_f32 v39, v70, v71
	ds_read_b128 v[68:71], v254 offset:51840
	s_waitcnt vmcnt(0) lgkmcnt(13)
	v_mfma_f32_32x32x16_f16 v[48:63], v[178:181], v[96:99], 0
	v_pk_max_f16 v21, v37, 0
	v_pk_max_f16 v20, v36, 0
	v_cvt_pk_f16_f32 v36, v64, v65
	v_cvt_pk_f16_f32 v37, v66, v67
	v_pk_max_f16 v65, v37, 0
	v_pk_max_f16 v64, v36, 0
	v_cvt_pk_f16_f32 v36, v72, v73
	s_waitcnt vmcnt(0) lgkmcnt(11)
	v_mfma_f32_32x32x16_f16 v[48:63], v[198:201], v[174:177], v[48:63]
	v_cvt_pk_f16_f32 v37, v74, v75
	ds_read_b128 v[72:75], v255 offset:1024
	v_pk_max_f16 v25, v25, 0
	v_pk_max_f16 v24, v24, 0
	v_pk_max_f16 v67, v39, 0
	v_pk_max_f16 v66, v38, 0
	ds_read_b128 v[160:163], v255 offset:3072
	v_mfma_f32_32x32x16_f16 v[48:63], v[194:197], v[128:131], v[48:63]
	v_cvt_pk_f16_f32 v38, v76, v77
	v_cvt_pk_f16_f32 v39, v78, v79
	v_pk_max_f16 v79, v39, 0
	v_pk_max_f16 v78, v38, 0
	v_pk_max_f16 v77, v37, 0
	v_pk_max_f16 v76, v36, 0
	v_cvt_pk_f16_f32 v36, v80, v81
	s_waitcnt vmcnt(0) lgkmcnt(12)
	v_mfma_f32_32x32x16_f16 v[48:63], v[40:43], v[20:23], v[48:63]
	v_cvt_pk_f16_f32 v38, v84, v85
	v_cvt_pk_f16_f32 v39, v86, v87
	ds_read_b128 v[84:87], v255 offset:5120
	v_cvt_pk_f16_f32 v37, v82, v83
	v_pk_max_f16 v80, v36, 0
	v_cvt_pk_f16_f32 v36, v92, v93
	s_mov_b32 s6, 0x20000
	s_waitcnt vmcnt(0) lgkmcnt(12)
	v_mfma_f32_32x32x16_f16 v[48:63], v[170:173], v[24:27], v[48:63]
	v_pk_max_f16 v83, v39, 0
	v_pk_max_f16 v81, v37, 0
	v_cvt_pk_f16_f32 v39, v90, v91
	v_cvt_pk_f16_f32 v37, v94, v95
	v_pk_max_f16 v90, v36, 0
	v_add_co_u32_e32 v36, vcc, s6, v156
	s_waitcnt vmcnt(0) lgkmcnt(10)
	v_mfma_f32_32x32x16_f16 v[48:63], v[166:169], v[64:67], v[48:63]
	v_pk_max_f16 v82, v38, 0
	v_pk_max_f16 v91, v37, 0
	v_addc_co_u32_e32 v37, vcc, 0, v157, vcc
	ds_read_b128 v[92:95], v255 offset:7168
	v_cvt_pk_f16_f32 v207, v44, v45
	v_and_b32_e32 v190, 0x7fff7fff, v207
	v_mfma_f32_32x32x16_f16 v[48:63], v[182:185], v[76:79], v[48:63]
	ds_read_b128 v[166:169], v255 offset:10240
	v_pk_fma_f16 v44, v190, s2, v164 op_sel_hi:[1,0,0]
	v_cvt_pk_f16_f32 v38, v88, v89
	v_pk_fma_f16 v44, v44, v190, s3 op_sel_hi:[1,1,0]
	v_pk_max_f16 v88, v38, 0
	v_pk_mul_f16 v44, v190, v44
	v_pk_add_f16 v38, v159, v153
	s_waitcnt vmcnt(0) lgkmcnt(10)
	v_mfma_f32_32x32x16_f16 v[48:63], v[116:119], v[80:83], v[48:63]
	ds_read_b128 v[116:119], v255 offset:26944
	v_exp_f16_e32 v45, v44
	v_exp_f16_sdwa v36, v44 dst_sel:DWORD dst_unused:UNUSED_PAD src0_sel:WORD_1
	v_pack_b32_f16 v37, v165, v206
	v_cvt_pk_f16_f32 v155, v46, v47
	v_pk_max_f16 v89, v39, 0
	v_pk_fma_f16 v153, v159, v37, v38 neg_lo:[1,0,0] neg_hi:[1,0,0]
	v_and_b32_e32 v159, 0x7fff7fff, v155
	s_waitcnt vmcnt(0) lgkmcnt(10)
	v_mfma_f32_32x32x16_f16 v[48:63], v[124:127], v[88:91], v[48:63]
	v_pk_fma_f16 v124, v159, s2, v164 op_sel_hi:[1,0,0]
	v_pack_b32_f16 v154, v45, v36
	v_pk_fma_f16 v124, v124, v159, s3 op_sel_hi:[1,1,0]
	v_pk_add_f16 v171, v190, v207
	v_pk_mul_f16 v165, v159, v124
	ds_read_b128 v[124:127], v255 offset:11264
	v_exp_f16_e32 v170, v165
	s_waitcnt vmcnt(0) lgkmcnt(10)
	v_mfma_f32_32x32x16_f16 v[32:47], v[32:35], v[96:99], 0
	v_exp_f16_sdwa v165, v165 dst_sel:DWORD dst_unused:UNUSED_PAD src0_sel:WORD_1
	v_pk_fma_f16 v154, v190, v154, v171 neg_lo:[1,0,0] neg_hi:[1,0,0]
	s_mov_b32 s6, 0x1e000
	v_cvt_pk_f16_f32 v4, v4, v5
	v_and_b32_e32 v5, 0x7fff7fff, v4
	v_cvt_pk_f16_f32 v56, v56, v57
	v_cvt_pk_f16_f32 v57, v58, v59
	s_waitcnt vmcnt(0) lgkmcnt(9)
	v_mfma_f32_32x32x16_f16 v[32:47], v[16:19], v[174:177], v[32:47]
	v_pack_b32_f16 v16, v170, v165
	ds_read_b128 v[170:173], v255 offset:12288
	v_add_co_u32_e32 v174, vcc, s6, v156
	v_cvt_pk_f16_f32 v18, v0, v1
	s_nop 0
	v_addc_co_u32_e32 v175, vcc, 0, v157, vcc
	s_waitcnt vmcnt(0) lgkmcnt(9)
	v_mfma_f32_32x32x16_f16 v[32:47], v[132:135], v[128:131], v[32:47]
	ds_read_b128 v[128:131], v255 offset:13312
	v_and_b32_e32 v19, 0x7fff7fff, v18
	ds_read_b128 v[132:135], v255 offset:14336
	v_pk_fma_f16 v0, v19, s2, v164 op_sel_hi:[1,0,0]
	v_pk_add_f16 v17, v159, v155
	v_pk_fma_f16 v0, v0, v19, s3 op_sel_hi:[1,1,0]
	s_mov_b32 s6, 0x1d000
	v_mfma_f32_32x32x16_f16 v[32:47], v[28:31], v[20:23], v[32:47]
	v_pk_mul_f16 v0, v19, v0
	v_pk_fma_f16 v155, v159, v16, v17 neg_lo:[1,0,0] neg_hi:[1,0,0]
	v_exp_f16_e32 v1, v0
	v_exp_f16_sdwa v0, v0 dst_sel:DWORD dst_unused:UNUSED_PAD src0_sel:WORD_1
	v_add_co_u32_e32 v16, vcc, s6, v156
	v_cvt_pk_f16_f32 v20, v2, v3
	s_nop 0
	v_addc_co_u32_e32 v17, vcc, 0, v157, vcc
	v_pack_b32_f16 v159, v1, v0
	s_waitcnt vmcnt(0) lgkmcnt(10)
	v_mfma_f32_32x32x16_f16 v[32:47], v[68:71], v[24:27], v[32:47]
	ds_read_b128 v[0:3], v255 offset:15360
	v_and_b32_e32 v21, 0x7fff7fff, v20
	v_pk_fma_f16 v22, v21, s2, v164 op_sel_hi:[1,0,0]
	v_pk_add_f16 v18, v19, v18
	v_pk_fma_f16 v22, v22, v21, s3 op_sel_hi:[1,1,0]
	v_pk_fma_f16 v68, v19, v159, v18 neg_lo:[1,0,0] neg_hi:[1,0,0]
	v_pk_mul_f16 v22, v21, v22
	s_waitcnt vmcnt(0) lgkmcnt(10)
	v_mfma_f32_32x32x16_f16 v[32:47], v[72:75], v[64:67], v[32:47]
	ds_read_b128 v[64:67], v255 offset:16384
	ds_read_b128 v[72:75], v255 offset:17728
	v_pk_fma_f16 v16, v5, s2, v164 op_sel_hi:[1,0,0]
	v_cvt_pk_f16_f32 v17, v50, v51
	v_pk_fma_f16 v70, v16, v5, s3 op_sel_hi:[1,1,0]
	v_cvt_pk_f16_f32 v16, v48, v49
	ds_read_b128 v[48:51], v255 offset:18752
	s_waitcnt vmcnt(0) lgkmcnt(12)
	v_mfma_f32_32x32x16_f16 v[32:47], v[160:163], v[76:79], v[32:47]
	v_exp_f16_e32 v23, v22
	v_exp_f16_sdwa v22, v22 dst_sel:DWORD dst_unused:UNUSED_PAD src0_sel:WORD_1
	ds_read_b128 v[76:79], v255 offset:19776
	v_pk_add_f16 v19, v21, v20
	v_cvt_pk_f16_f32 v58, v60, v61
	v_pack_b32_f16 v18, v23, v22
	v_pk_fma_f16 v69, v21, v18, v19 neg_lo:[1,0,0] neg_hi:[1,0,0]
	s_waitcnt vmcnt(0) lgkmcnt(12)
	v_mfma_f32_32x32x16_f16 v[32:47], v[84:87], v[80:83], v[32:47]
	v_cvt_pk_f16_f32 v18, v52, v53
	v_cvt_pk_f16_f32 v19, v54, v55
	v_pk_max_f16 v55, v19, 0
	v_pk_max_f16 v54, v18, 0
	v_pk_max_f16 v53, v17, 0
	v_pk_max_f16 v52, v16, 0
	v_cvt_pk_f16_f32 v59, v62, v63
	s_waitcnt vmcnt(0) lgkmcnt(9)
	v_mfma_f32_32x32x16_f16 v[16:31], v[116:119], v[96:99], 0
	ds_read_b128 v[60:63], v255 offset:20800
	v_pk_max_f16 v59, v59, 0
	v_pk_max_f16 v58, v58, 0
	v_pk_max_f16 v57, v57, 0
	v_pk_max_f16 v56, v56, 0
	v_cvt_pk_f16_f32 v6, v6, v7
	v_and_b32_e32 v7, 0x7fff7fff, v6
	v_mfma_f32_32x32x16_f16 v[32:47], v[92:95], v[88:91], v[32:47]
	v_pk_add_f16 v4, v5, v4
	s_mov_b32 s6, 0x1f000
	v_mfma_f32_32x32x16_f16 v[16:31], v[166:169], v[52:55], v[16:31]
	s_nop 8
	v_cvt_pk_f16_f32 v32, v32, v33
	v_cvt_pk_f16_f32 v33, v34, v35
	v_cvt_pk_f16_f32 v34, v36, v37
	v_cvt_pk_f16_f32 v35, v38, v39
	ds_read_b128 v[36:39], v255 offset:21824
	v_pk_max_f16 v35, v35, 0
	v_pk_max_f16 v34, v34, 0
	s_waitcnt vmcnt(0) lgkmcnt(10)
	v_mfma_f32_32x32x16_f16 v[16:31], v[124:127], v[56:59], v[16:31]
	v_pk_max_f16 v33, v33, 0
	v_pk_max_f16 v32, v32, 0
	v_cvt_pk_f16_f32 v40, v40, v41
	v_add_co_u32_e32 v56, vcc, s6, v156
	s_nop 1
	v_addc_co_u32_e32 v57, vcc, 0, v157, vcc
	s_waitcnt vmcnt(0) lgkmcnt(9)
	v_mfma_f32_32x32x16_f16 v[16:31], v[170:173], v[32:35], v[16:31]
	v_cvt_pk_f16_f32 v32, v42, v43
	v_cvt_pk_f16_f32 v33, v44, v45
	v_cvt_pk_f16_f32 v34, v46, v47
	v_pk_max_f16 v35, v34, 0
	v_pk_max_f16 v34, v33, 0
	v_pk_max_f16 v33, v32, 0
	v_pk_max_f16 v32, v40, 0
	ds_read_b128 v[52:55], v255 offset:22848
	s_waitcnt vmcnt(0) lgkmcnt(9)
	v_mfma_f32_32x32x16_f16 v[16:31], v[128:131], v[32:35], v[16:31]
	v_pk_fma_f16 v34, v7, s2, v164 op_sel_hi:[1,0,0]
	v_pk_mul_f16 v32, v5, v70
	v_pk_fma_f16 v34, v34, v7, s3 op_sel_hi:[1,1,0]
	v_exp_f16_e32 v33, v32
	v_exp_f16_sdwa v32, v32 dst_sel:DWORD dst_unused:UNUSED_PAD src0_sel:WORD_1
	v_pk_mul_f16 v34, v7, v34
	v_pack_b32_f16 v32, v33, v32
	s_waitcnt vmcnt(0) lgkmcnt(8)
	v_mfma_f32_32x32x16_f16 v[16:31], v[132:135], v[120:123], v[16:31]
	v_exp_f16_e32 v35, v34
	v_exp_f16_sdwa v34, v34 dst_sel:DWORD dst_unused:UNUSED_PAD src0_sel:WORD_1
	v_pk_fma_f16 v70, v5, v32, v4 neg_lo:[1,0,0] neg_hi:[1,0,0]
	v_pack_b32_f16 v4, v35, v34
	s_waitcnt vmcnt(0) lgkmcnt(7)
	v_mfma_f32_32x32x16_f16 v[16:31], v[0:3], v[136:139], v[16:31]
	v_pk_add_f16 v0, v7, v6
	s_nop 0
	v_pk_fma_f16 v71, v7, v4, v0 neg_lo:[1,0,0] neg_hi:[1,0,0]
	v_cvt_pk_f16_f32 v0, v8, v9
	v_and_b32_e32 v1, 0x7fff7fff, v0
	v_cvt_pk_f16_f32 v4, v10, v11
	v_pk_fma_f16 v2, v1, s2, v164 op_sel_hi:[1,0,0]
	s_waitcnt vmcnt(0) lgkmcnt(6)
	v_mfma_f32_32x32x16_f16 v[16:31], v[64:67], v[140:143], v[16:31]
	v_and_b32_e32 v5, 0x7fff7fff, v4
	v_pk_fma_f16 v2, v2, v1, s3 op_sel_hi:[1,1,0]
	v_pk_fma_f16 v6, v5, s2, v164 op_sel_hi:[1,0,0]
	v_pk_mul_f16 v2, v1, v2
	v_pk_fma_f16 v6, v6, v5, s3 op_sel_hi:[1,1,0]
	v_exp_f16_e32 v3, v2
	v_exp_f16_sdwa v2, v2 dst_sel:DWORD dst_unused:UNUSED_PAD src0_sel:WORD_1
	s_waitcnt vmcnt(0) lgkmcnt(5)
	v_mfma_f32_32x32x16_f16 v[16:31], v[72:75], v[144:147], v[16:31]
	v_pk_mul_f16 v6, v5, v6
	v_pk_add_f16 v0, v1, v0
	v_exp_f16_e32 v7, v6
	v_exp_f16_sdwa v6, v6 dst_sel:DWORD dst_unused:UNUSED_PAD src0_sel:WORD_1
	v_pack_b32_f16 v2, v3, v2
	v_pk_fma_f16 v0, v1, v2, v0 neg_lo:[1,0,0] neg_hi:[1,0,0]
	v_pk_add_f16 v2, v5, v4
	s_waitcnt vmcnt(0) lgkmcnt(4)
	v_mfma_f32_32x32x16_f16 v[16:31], v[48:51], v[148:151], v[16:31]
	v_pack_b32_f16 v1, v7, v6
	v_pk_fma_f16 v1, v5, v1, v2 neg_lo:[1,0,0] neg_hi:[1,0,0]
	v_cvt_pk_f16_f32 v2, v12, v13
	v_and_b32_e32 v3, 0x7fff7fff, v2
	v_cvt_pk_f16_f32 v6, v14, v15
	v_pk_fma_f16 v4, v3, s2, v164 op_sel_hi:[1,0,0]
	v_and_b32_e32 v7, 0x7fff7fff, v6
	s_waitcnt vmcnt(0) lgkmcnt(3)
	v_mfma_f32_32x32x16_f16 v[16:31], v[76:79], v[152:155], v[16:31]
	v_pk_fma_f16 v4, v4, v3, s3 op_sel_hi:[1,1,0]
	v_pk_fma_f16 v8, v7, s2, v164 op_sel_hi:[1,0,0]
	v_pk_mul_f16 v4, v3, v4
	v_pk_fma_f16 v8, v8, v7, s3 op_sel_hi:[1,1,0]
	v_exp_f16_e32 v5, v4
	v_exp_f16_sdwa v4, v4 dst_sel:DWORD dst_unused:UNUSED_PAD src0_sel:WORD_1
	v_pk_mul_f16 v8, v7, v8
	s_waitcnt vmcnt(0) lgkmcnt(2)
	v_mfma_f32_32x32x16_f16 v[16:31], v[60:63], v[68:71], v[16:31]
	v_exp_f16_e32 v9, v8
	v_exp_f16_sdwa v8, v8 dst_sel:DWORD dst_unused:UNUSED_PAD src0_sel:WORD_1
	v_pack_b32_f16 v4, v5, v4
	v_pk_add_f16 v2, v3, v2
	s_nop 0
	v_pk_fma_f16 v2, v3, v4, v2 neg_lo:[1,0,0] neg_hi:[1,0,0]
	v_pack_b32_f16 v3, v9, v8
	v_pk_add_f16 v4, v7, v6
	s_nop 0
	v_pk_fma_f16 v3, v7, v3, v4 neg_lo:[1,0,0] neg_hi:[1,0,0]
	ds_read_b128 v[4:7], v255 offset:24896
	s_waitcnt vmcnt(0) lgkmcnt(2)
	v_mfma_f32_32x32x16_f16 v[16:31], v[36:39], v[0:3], v[16:31]
	ds_read_b128 v[0:3], v255 offset:23872
	s_waitcnt vmcnt(0) lgkmcnt(2)
	v_mfma_f32_32x32x16_f16 v[16:31], v[52:55], v[104:107], v[16:31]
	s_waitcnt vmcnt(0) lgkmcnt(0)
	v_mfma_f32_32x32x16_f16 v[16:31], v[0:3], v[100:103], v[16:31]
	ds_read_b128 v[0:3], v255 offset:25920
	v_mfma_f32_32x32x16_f16 v[16:31], v[4:7], v[112:115], v[16:31]
	s_waitcnt vmcnt(0) lgkmcnt(0)
	v_mfma_f32_32x32x16_f16 v[16:31], v[0:3], v[108:111], v[16:31]
	s_nop 11
	ds_bpermute_b32 v3, v209, v16
	ds_bpermute_b32 v2, v209, v17
	ds_bpermute_b32 v1, v209, v18
	ds_bpermute_b32 v0, v209, v19
	s_and_saveexec_b64 s[2:3], s[0:1]
	s_cbranch_execz .LBB0_33
	v_max_f32_e32 v4, v17, v17
	v_max_f32_e32 v5, v16, v16
	v_max_f32_e32 v4, v5, v4
	v_max_f32_e32 v5, v19, v19
	v_max_f32_e32 v6, v18, v18
	v_max_f32_e32 v5, v6, v5
	s_waitcnt vmcnt(0) lgkmcnt(3)
	v_max3_f32 v6, v4, v5, v3
	v_sub_f32_e32 v4, v16, v6
	v_sub_f32_e32 v5, v17, v6
	v_sub_f32_e32 v7, v18, v6
	v_mul_f32_e32 v4, 0x3fb8aa3b, v4
	v_mul_f32_e32 v5, 0x3fb8aa3b, v5
	v_mul_f32_e32 v7, 0x3fb8aa3b, v7
	v_exp_f32_e32 v4, v4
	v_exp_f32_e32 v5, v5
	v_exp_f32_e32 v9, v7
	v_sub_f32_e32 v7, v19, v6
	v_mul_f32_e32 v7, 0x3fb8aa3b, v7
	v_sub_f32_e32 v6, v3, v6
	v_exp_f32_e32 v7, v7
	v_mul_f32_e32 v6, 0x3fb8aa3b, v6
	v_exp_f32_e32 v6, v6
	v_add_f32_e32 v8, v4, v5
	v_add_f32_e32 v8, v9, v8
	v_add_f32_e32 v8, v7, v8
	v_add_f32_e32 v8, v6, v8
	v_rcp_f32_e32 v8, v8
	s_waitcnt vmcnt(0) lgkmcnt(1)
	v_mul_f32_e32 v1, 0xbfb8aa3b, v1
	v_exp_f32_e32 v1, v1
	s_mov_b32 s1, 0x403fba14
	v_pk_mul_f32 v[6:7], v[6:7], v[8:9] op_sel_hi:[1,0]
	s_mov_b32 s0, 0x40f33a98
	v_pk_mul_f32 v[20:21], v[4:5], v[8:9] op_sel_hi:[1,0]
	v_pk_mul_f32 v[14:15], v[6:7], s[0:1]
	s_mov_b32 s0, 0x411e74af
	v_add_f32_e32 v4, v20, v21
	v_mul_f32_e32 v12, v9, v8
	v_fmac_f32_e32 v4, v9, v8
	v_pk_mul_f32 v[8:9], v[20:21], s[0:1]
	s_mov_b32 s3, 0x4108466c
	s_mov_b32 s2, s1
	v_add_f32_e32 v1, 1.0, v1
	v_mul_f32_e32 v13, 0x411e74af, v6
	v_pk_fma_f32 v[8:9], v[20:21], s[2:3], v[8:9] op_sel:[0,0,1] op_sel_hi:[1,1,0]
	s_mov_b32 s2, 0x40dd0c55
	s_mov_b32 s3, s0
	v_max_f32_e32 v2, v2, v2
	v_rcp_f32_e32 v1, v1
	v_mul_f32_e32 v7, 0x40c6de12, v7
	v_pk_fma_f32 v[8:9], v[12:13], s[2:3], v[8:9] op_sel_hi:[0,1,1]
	v_mov_b32_e32 v6, v15
	v_max_f32_e32 v2, 0xc1400000, v2
	v_pk_add_f32 v[6:7], v[6:7], v[8:9]
	v_mov_b32_e32 v15, v13
	v_min_f32_e32 v2, 0x41400000, v2
	v_pk_add_f32 v[6:7], v[14:15], v[6:7]
	s_mov_b32 s4, 0xbfb8aa3b
	v_mul_f32_e32 v4, v2, v4
	v_sub_f32_e32 v2, v7, v6
	v_fmac_f32_e32 v6, v1, v2
	s_waitcnt vmcnt(0) lgkmcnt(0)
	v_mul_f32_e64 v1, |v0|, s4
	v_exp_f32_e32 v1, v1
	v_max_f32_e32 v0, v0, v0
	v_mov_b32_e32 v2, 0x411e74af
	v_max_f32_e32 v0, 0, v0
	v_add_f32_e32 v1, 1.0, v1
	v_log_f32_e32 v1, v1
	v_med3_f32 v2, v6, s1, v2
	v_mul_f32_e32 v2, 0x3fb8aa3b, v2
	v_exp_f32_e32 v5, v2
	v_fmamk_f32 v0, v1, 0x3f317218, v0
	v_add_f32_e32 v0, 0x3dcccccd, v0
	v_max_f32_e32 v0, 0x3dcccccd, v0
	v_min_f32_e32 v6, 0x41200000, v0
	v_lshlrev_b32_e32 v0, 3, v158
	v_mov_b32_e32 v10, s38
	v_mov_b32_e32 v11, s39
	v_ashrrev_i32_e32 v1, 31, v0
	v_lshl_add_u64 v[8:9], v[0:1], 2, v[10:11]
	v_mov_b32_e32 v7, v16
	v_pk_mov_b32 v[0:1], v[16:17], v[18:19] op_sel:[1,0]
	v_mov_b32_e32 v2, v19
	global_store_dwordx4 v[8:9], v[4:7], off
	global_store_dwordx4 v[8:9], v[0:3], off offset:16
